# v102 + k6 LN1 row statistics: ds_bpermute shuffles replaced by v_permlane16/32_swap pairs; k3 statistics: LDS waits after the per-group ds_write dropped (only the final one before the barrier kept)
# baseline (speedup 1.0000x reference)
.LBB0_810:
	v_and_b32_e32 v133, 64, v249
	v_xor_b32_e32 v132, 16, v249
	v_add_u32_e32 v136, 64, v133
	v_cmp_lt_i32_e32 vcc, v132, v136
	v_mul_f32_e32 v134, v129, v129
	v_fmac_f32_e32 v134, v128, v128
	v_cndmask_b32_e32 v132, v249, v132, vcc
	v_lshlrev_b32_e32 v137, 2, v132
	v_add_f32_e32 v132, 0, v128
	v_add_f32_e32 v132, v129, v132
	v_add_f32_e32 v132, v130, v132
	v_add_f32_e32 v132, v131, v132
	v_add_f32_e32 v135, v124, v132
	v_mov_b32_e32 v132, v124
	v_mov_b32_e32 v133, v131
	v_fmac_f32_e32 v134, v130, v130
	v_pk_mul_f32 v[132:133], v[132:133], v[132:133]
	s_mov_b64 s[58:59], s[44:45]
	v_add_f32_e32 v133, v133, v134
	v_add_f32_e32 v138, v132, v133
	v_add_f32_e32 v132, v125, v135
	v_add_f32_e32 v139, v126, v132
	v_pk_mul_f32 v[132:133], v[126:127], v[126:127]
	v_pk_mul_f32 v[134:135], v[124:125], v[124:125]
	s_nop 0
	v_add_f32_e32 v133, v135, v138
	v_add_f32_e32 v134, v132, v133
	v_add_f32_e32 v132, v127, v139
	v_add_f32_e32 v135, v132, v120
	v_pk_mov_b32 v[132:133], v[126:127], v[120:121] op_sel:[1,0]
	s_nop 0
	v_pk_mul_f32 v[132:133], v[132:133], v[132:133]
	s_nop 0
	v_add_f32_e32 v132, v132, v134
	v_add_f32_e32 v138, v132, v133
	v_add_f32_e32 v132, v121, v135
	v_add_f32_e32 v139, v122, v132
	v_pk_mul_f32 v[132:133], v[122:123], v[122:123]
	v_pk_mul_f32 v[134:135], v[120:121], v[120:121]
	s_nop 0
	v_add_f32_e32 v133, v135, v138
	v_add_f32_e32 v134, v132, v133
	v_add_f32_e32 v132, v123, v139
	v_add_f32_e32 v135, v116, v132
	v_mov_b32_e32 v132, v116
	v_mov_b32_e32 v133, v123
	v_pk_mul_f32 v[132:133], v[132:133], v[132:133]
	v_pk_mul_f32 v[138:139], v[116:117], v[116:117]
	v_add_f32_e32 v133, v133, v134
	v_add_f32_e32 v133, v132, v133
	v_add_f32_e32 v132, v117, v135
	v_pk_mul_f32 v[134:135], v[118:119], v[118:119]
	v_add_f32_e32 v133, v139, v133
	v_add_f32_e32 v132, v118, v132
	v_add_f32_e32 v135, v134, v133
	v_mul_f32_e32 v133, v119, v119
	v_mov_b32_e32 v134, v119
	v_pk_add_f32 v[132:133], v[134:135], v[132:133]
	v_mov_b32_e32 v134, v132
	v_mov_b32_e32 v135, v133
	s_nop 1
	v_permlane16_swap_b32_e32 v134, v132
	v_permlane16_swap_b32_e32 v135, v133
	v_xor_b32_e32 v138, 32, v249
	v_cmp_lt_i32_e32 vcc, v138, v136
	v_pk_add_f32 v[132:133], v[132:133], v[134:135]
	v_cndmask_b32_e32 v136, v249, v138, vcc
	v_lshlrev_b32_e32 v139, 2, v136
	v_mov_b32_e32 v134, v132
	v_mov_b32_e32 v135, v133
	s_nop 1
	v_permlane32_swap_b32_e32 v134, v132
	v_permlane32_swap_b32_e32 v135, v133
	v_mov_b32_e32 v136, v205
	s_nop 0
	v_lshl_add_u32 v138, v136, 5, s94
	s_and_saveexec_b64 s[26:27], s[38:39]
	s_cbranch_execz .LBB0_812
	v_pk_add_f32 v[132:133], v[132:133], v[134:135]
	ds_write_b64 v138, v[132:133]
.LBB0_812:
	s_or_b64 exec, exec, s[26:27]
	v_add_f32_e32 v132, 0, v112
	v_add_f32_e32 v132, v113, v132
	v_add_f32_e32 v132, v114, v132
	v_mul_f32_e32 v134, v113, v113
	v_add_f32_e32 v132, v115, v132
	v_fmac_f32_e32 v134, v112, v112
	v_add_f32_e32 v135, v108, v132
	v_mov_b32_e32 v132, v108
	v_mov_b32_e32 v133, v115
	v_fmac_f32_e32 v134, v114, v114
	v_pk_mul_f32 v[132:133], v[132:133], v[132:133]
	s_nop 0
	v_add_f32_e32 v133, v133, v134
	v_add_f32_e32 v140, v132, v133
	v_add_f32_e32 v132, v109, v135
	v_add_f32_e32 v141, v110, v132
	v_pk_mul_f32 v[132:133], v[110:111], v[110:111]
	v_pk_mul_f32 v[134:135], v[108:109], v[108:109]
	s_nop 0
	v_add_f32_e32 v133, v135, v140
	v_add_f32_e32 v134, v132, v133
	v_add_f32_e32 v132, v111, v141
	v_add_f32_e32 v135, v132, v104
	v_pk_mov_b32 v[132:133], v[110:111], v[104:105] op_sel:[1,0]
	s_nop 0
	v_pk_mul_f32 v[132:133], v[132:133], v[132:133]
	s_nop 0
	v_add_f32_e32 v132, v132, v134
	v_add_f32_e32 v140, v132, v133
	v_add_f32_e32 v132, v105, v135
	v_add_f32_e32 v141, v106, v132
	v_pk_mul_f32 v[132:133], v[106:107], v[106:107]
	v_pk_mul_f32 v[134:135], v[104:105], v[104:105]
	s_nop 0
	v_add_f32_e32 v133, v135, v140
	v_add_f32_e32 v134, v132, v133
	v_add_f32_e32 v132, v107, v141
	v_add_f32_e32 v135, v100, v132
	v_mov_b32_e32 v132, v100
	v_mov_b32_e32 v133, v107
	v_pk_mul_f32 v[132:133], v[132:133], v[132:133]
	v_pk_mul_f32 v[140:141], v[100:101], v[100:101]
	v_add_f32_e32 v133, v133, v134
	v_add_f32_e32 v133, v132, v133
	v_add_f32_e32 v132, v101, v135
	v_pk_mul_f32 v[134:135], v[102:103], v[102:103]
	v_add_f32_e32 v133, v141, v133
	v_add_f32_e32 v132, v102, v132
	v_add_f32_e32 v135, v134, v133
	v_mul_f32_e32 v133, v103, v103
	v_mov_b32_e32 v134, v103
	v_pk_add_f32 v[132:133], v[134:135], v[132:133]
	v_mov_b32_e32 v134, v132
	v_mov_b32_e32 v135, v133
	s_nop 1
	v_permlane16_swap_b32_e32 v134, v132
	v_permlane16_swap_b32_e32 v135, v133
	v_pk_add_f32 v[132:133], v[132:133], v[134:135]
	v_mov_b32_e32 v134, v132
	v_mov_b32_e32 v135, v133
	s_nop 1
	v_permlane32_swap_b32_e32 v134, v132
	v_permlane32_swap_b32_e32 v135, v133
	s_and_saveexec_b64 s[26:27], s[38:39]
	s_cbranch_execz .LBB0_814
	v_pk_add_f32 v[132:133], v[132:133], v[134:135]
	ds_write_b64 v138, v[132:133] offset:512
.LBB0_814:
	s_or_b64 exec, exec, s[26:27]
	v_add_f32_e32 v132, 0, v96
	v_add_f32_e32 v132, v97, v132
	v_add_f32_e32 v132, v98, v132
	v_mul_f32_e32 v134, v97, v97
	v_add_f32_e32 v132, v99, v132
	v_fmac_f32_e32 v134, v96, v96
	v_add_f32_e32 v135, v92, v132
	v_mov_b32_e32 v132, v92
	v_mov_b32_e32 v133, v99
	v_fmac_f32_e32 v134, v98, v98
	v_pk_mul_f32 v[132:133], v[132:133], v[132:133]
	s_nop 0
	v_add_f32_e32 v133, v133, v134
	v_add_f32_e32 v140, v132, v133
	v_add_f32_e32 v132, v93, v135
	v_add_f32_e32 v141, v94, v132
	v_pk_mul_f32 v[132:133], v[94:95], v[94:95]
	v_pk_mul_f32 v[134:135], v[92:93], v[92:93]
	s_nop 0
	v_add_f32_e32 v133, v135, v140
	v_add_f32_e32 v134, v132, v133
	v_add_f32_e32 v132, v95, v141
	v_add_f32_e32 v135, v132, v88
	v_pk_mov_b32 v[132:133], v[94:95], v[88:89] op_sel:[1,0]
	s_nop 0
	v_pk_mul_f32 v[132:133], v[132:133], v[132:133]
	s_nop 0
	v_add_f32_e32 v132, v132, v134
	v_add_f32_e32 v140, v132, v133
	v_add_f32_e32 v132, v89, v135
	v_add_f32_e32 v141, v90, v132
	v_pk_mul_f32 v[132:133], v[90:91], v[90:91]
	v_pk_mul_f32 v[134:135], v[88:89], v[88:89]
	s_nop 0
	v_add_f32_e32 v133, v135, v140
	v_add_f32_e32 v134, v132, v133
	v_add_f32_e32 v132, v91, v141
	v_add_f32_e32 v135, v84, v132
	v_mov_b32_e32 v132, v84
	v_mov_b32_e32 v133, v91
	v_pk_mul_f32 v[132:133], v[132:133], v[132:133]
	v_pk_mul_f32 v[140:141], v[84:85], v[84:85]
	v_add_f32_e32 v133, v133, v134
	v_add_f32_e32 v133, v132, v133
	v_add_f32_e32 v132, v85, v135
	v_pk_mul_f32 v[134:135], v[86:87], v[86:87]
	v_add_f32_e32 v133, v141, v133
	v_add_f32_e32 v132, v86, v132
	v_add_f32_e32 v135, v134, v133
	v_mul_f32_e32 v133, v87, v87
	v_mov_b32_e32 v134, v87
	v_pk_add_f32 v[132:133], v[134:135], v[132:133]
	v_mov_b32_e32 v134, v132
	v_mov_b32_e32 v135, v133
	s_nop 1
	v_permlane16_swap_b32_e32 v134, v132
	v_permlane16_swap_b32_e32 v135, v133
	v_pk_add_f32 v[132:133], v[132:133], v[134:135]
	v_mov_b32_e32 v134, v132
	v_mov_b32_e32 v135, v133
	s_nop 1
	v_permlane32_swap_b32_e32 v134, v132
	v_permlane32_swap_b32_e32 v135, v133
	s_and_saveexec_b64 s[26:27], s[38:39]
	s_cbranch_execz .LBB0_816
	v_pk_add_f32 v[132:133], v[132:133], v[134:135]
	ds_write_b64 v138, v[132:133] offset:1024
.LBB0_816:
	s_or_b64 exec, exec, s[26:27]
	v_add_f32_e32 v132, 0, v80
	v_add_f32_e32 v132, v81, v132
	v_add_f32_e32 v132, v82, v132
	v_mul_f32_e32 v134, v81, v81
	v_add_f32_e32 v132, v83, v132
	v_fmac_f32_e32 v134, v80, v80
	v_add_f32_e32 v135, v76, v132
	v_mov_b32_e32 v132, v76
	v_mov_b32_e32 v133, v83
	v_fmac_f32_e32 v134, v82, v82
	v_pk_mul_f32 v[132:133], v[132:133], v[132:133]
	s_nop 0
	v_add_f32_e32 v133, v133, v134
	v_add_f32_e32 v140, v132, v133
	v_add_f32_e32 v132, v77, v135
	v_add_f32_e32 v141, v78, v132
	v_pk_mul_f32 v[132:133], v[78:79], v[78:79]
	v_pk_mul_f32 v[134:135], v[76:77], v[76:77]
	s_nop 0
	v_add_f32_e32 v133, v135, v140
	v_add_f32_e32 v134, v132, v133
	v_add_f32_e32 v132, v79, v141
	v_add_f32_e32 v135, v132, v72
	v_pk_mov_b32 v[132:133], v[78:79], v[72:73] op_sel:[1,0]
	s_nop 0
	v_pk_mul_f32 v[132:133], v[132:133], v[132:133]
	s_nop 0
	v_add_f32_e32 v132, v132, v134
	v_add_f32_e32 v140, v132, v133
	v_add_f32_e32 v132, v73, v135
	v_add_f32_e32 v141, v74, v132
	v_pk_mul_f32 v[132:133], v[74:75], v[74:75]
	v_pk_mul_f32 v[134:135], v[72:73], v[72:73]
	s_nop 0
	v_add_f32_e32 v133, v135, v140
	v_add_f32_e32 v134, v132, v133
	v_add_f32_e32 v132, v75, v141
	v_add_f32_e32 v135, v68, v132
	v_mov_b32_e32 v132, v68
	v_mov_b32_e32 v133, v75
	v_pk_mul_f32 v[132:133], v[132:133], v[132:133]
	v_pk_mul_f32 v[140:141], v[68:69], v[68:69]
	v_add_f32_e32 v133, v133, v134
	v_add_f32_e32 v133, v132, v133
	v_add_f32_e32 v132, v69, v135
	v_pk_mul_f32 v[134:135], v[70:71], v[70:71]
	v_add_f32_e32 v133, v141, v133
	v_add_f32_e32 v132, v70, v132
	v_add_f32_e32 v135, v134, v133
	v_mul_f32_e32 v133, v71, v71
	v_mov_b32_e32 v134, v71
	v_pk_add_f32 v[132:133], v[134:135], v[132:133]
	v_mov_b32_e32 v134, v132
	v_mov_b32_e32 v135, v133
	s_nop 1
	v_permlane16_swap_b32_e32 v134, v132
	v_permlane16_swap_b32_e32 v135, v133
	v_pk_add_f32 v[132:133], v[132:133], v[134:135]
	v_mov_b32_e32 v134, v132
	v_mov_b32_e32 v135, v133
	s_nop 1
	v_permlane32_swap_b32_e32 v134, v132
	v_permlane32_swap_b32_e32 v135, v133
	s_and_saveexec_b64 s[26:27], s[38:39]
	s_cbranch_execz .LBB0_818
	v_pk_add_f32 v[132:133], v[132:133], v[134:135]
	ds_write_b64 v138, v[132:133] offset:1536
.LBB0_818:
	s_or_b64 exec, exec, s[26:27]
	v_add_f32_e32 v132, 0, v62
	v_add_f32_e32 v132, v63, v132
	v_add_f32_e32 v132, v64, v132
	v_mul_f32_e32 v134, v63, v63
	v_add_f32_e32 v132, v65, v132
	v_fmac_f32_e32 v134, v62, v62
	v_add_f32_e32 v135, v58, v132
	v_mov_b32_e32 v132, v58
	v_mov_b32_e32 v133, v65
	v_fmac_f32_e32 v134, v64, v64
	v_pk_mul_f32 v[132:133], v[132:133], v[132:133]
	s_nop 0
	v_add_f32_e32 v133, v133, v134
	v_add_f32_e32 v140, v132, v133
	v_add_f32_e32 v132, v59, v135
	v_add_f32_e32 v141, v60, v132
	v_pk_mul_f32 v[132:133], v[60:61], v[60:61]
	v_pk_mul_f32 v[134:135], v[58:59], v[58:59]
	s_nop 0
	v_add_f32_e32 v133, v135, v140
	v_add_f32_e32 v134, v132, v133
	v_add_f32_e32 v132, v61, v141
	v_add_f32_e32 v135, v132, v54
	v_pk_mov_b32 v[132:133], v[60:61], v[54:55] op_sel:[1,0]
	s_nop 0
	v_pk_mul_f32 v[132:133], v[132:133], v[132:133]
	s_nop 0
	v_add_f32_e32 v132, v132, v134
	v_add_f32_e32 v140, v132, v133
	v_add_f32_e32 v132, v55, v135
	v_add_f32_e32 v141, v56, v132
	v_pk_mul_f32 v[132:133], v[56:57], v[56:57]
	v_pk_mul_f32 v[134:135], v[54:55], v[54:55]
	s_nop 0
	v_add_f32_e32 v133, v135, v140
	v_add_f32_e32 v134, v132, v133
	v_add_f32_e32 v132, v57, v141
	v_add_f32_e32 v135, v50, v132
	v_mov_b32_e32 v132, v50
	v_mov_b32_e32 v133, v57
	v_pk_mul_f32 v[132:133], v[132:133], v[132:133]
	v_pk_mul_f32 v[140:141], v[50:51], v[50:51]
	v_add_f32_e32 v133, v133, v134
	v_add_f32_e32 v133, v132, v133
	v_add_f32_e32 v132, v51, v135
	v_pk_mul_f32 v[134:135], v[52:53], v[52:53]
	v_add_f32_e32 v133, v141, v133
	v_add_f32_e32 v132, v52, v132
	v_add_f32_e32 v135, v134, v133
	v_mul_f32_e32 v133, v53, v53
	v_mov_b32_e32 v134, v53
	v_pk_add_f32 v[132:133], v[134:135], v[132:133]
	v_mov_b32_e32 v134, v132
	v_mov_b32_e32 v135, v133
	s_nop 1
	v_permlane16_swap_b32_e32 v134, v132
	v_permlane16_swap_b32_e32 v135, v133
	v_pk_add_f32 v[132:133], v[132:133], v[134:135]
	v_mov_b32_e32 v134, v132
	v_mov_b32_e32 v135, v133
	s_nop 1
	v_permlane32_swap_b32_e32 v134, v132
	v_permlane32_swap_b32_e32 v135, v133
	s_and_saveexec_b64 s[26:27], s[38:39]
	s_cbranch_execz .LBB0_820
	v_pk_add_f32 v[132:133], v[132:133], v[134:135]
	ds_write_b64 v138, v[132:133] offset:4096
.LBB0_820:
	s_or_b64 exec, exec, s[26:27]
	v_add_f32_e32 v132, 0, v46
	v_add_f32_e32 v132, v47, v132
	v_add_f32_e32 v132, v48, v132
	v_mul_f32_e32 v134, v47, v47
	v_add_f32_e32 v132, v49, v132
	v_fmac_f32_e32 v134, v46, v46
	v_add_f32_e32 v135, v42, v132
	v_mov_b32_e32 v132, v42
	v_mov_b32_e32 v133, v49
	v_fmac_f32_e32 v134, v48, v48
	v_pk_mul_f32 v[132:133], v[132:133], v[132:133]
	s_nop 0
	v_add_f32_e32 v133, v133, v134
	v_add_f32_e32 v140, v132, v133
	v_add_f32_e32 v132, v43, v135
	v_add_f32_e32 v141, v44, v132
	v_pk_mul_f32 v[132:133], v[44:45], v[44:45]
	v_pk_mul_f32 v[134:135], v[42:43], v[42:43]
	s_nop 0
	v_add_f32_e32 v133, v135, v140
	v_add_f32_e32 v134, v132, v133
	v_add_f32_e32 v132, v45, v141
	v_add_f32_e32 v135, v132, v38
	v_pk_mov_b32 v[132:133], v[44:45], v[38:39] op_sel:[1,0]
	s_nop 0
	v_pk_mul_f32 v[132:133], v[132:133], v[132:133]
	s_nop 0
	v_add_f32_e32 v132, v132, v134
	v_add_f32_e32 v140, v132, v133
	v_add_f32_e32 v132, v39, v135
	v_add_f32_e32 v141, v40, v132
	v_pk_mul_f32 v[132:133], v[40:41], v[40:41]
	v_pk_mul_f32 v[134:135], v[38:39], v[38:39]
	s_nop 0
	v_add_f32_e32 v133, v135, v140
	v_add_f32_e32 v134, v132, v133
	v_add_f32_e32 v132, v41, v141
	v_add_f32_e32 v135, v34, v132
	v_mov_b32_e32 v132, v34
	v_mov_b32_e32 v133, v41
	v_pk_mul_f32 v[132:133], v[132:133], v[132:133]
	v_pk_mul_f32 v[140:141], v[34:35], v[34:35]
	v_add_f32_e32 v133, v133, v134
	v_add_f32_e32 v133, v132, v133
	v_add_f32_e32 v132, v35, v135
	v_pk_mul_f32 v[134:135], v[36:37], v[36:37]
	v_add_f32_e32 v133, v141, v133
	v_add_f32_e32 v132, v36, v132
	v_add_f32_e32 v135, v134, v133
	v_mul_f32_e32 v133, v37, v37
	v_mov_b32_e32 v134, v37
	v_pk_add_f32 v[132:133], v[134:135], v[132:133]
	v_mov_b32_e32 v134, v132
	v_mov_b32_e32 v135, v133
	s_nop 1
	v_permlane16_swap_b32_e32 v134, v132
	v_permlane16_swap_b32_e32 v135, v133
	v_pk_add_f32 v[132:133], v[132:133], v[134:135]
	v_mov_b32_e32 v134, v132
	v_mov_b32_e32 v135, v133
	s_nop 1
	v_permlane32_swap_b32_e32 v134, v132
	v_permlane32_swap_b32_e32 v135, v133
	s_and_saveexec_b64 s[26:27], s[38:39]
	s_cbranch_execz .LBB0_822
	v_pk_add_f32 v[132:133], v[132:133], v[134:135]
	ds_write_b64 v138, v[132:133] offset:4608
.LBB0_822:
	s_or_b64 exec, exec, s[26:27]
	v_add_f32_e32 v132, 0, v30
	v_add_f32_e32 v132, v31, v132
	v_add_f32_e32 v132, v32, v132
	v_mul_f32_e32 v134, v31, v31
	v_add_f32_e32 v132, v33, v132
	v_fmac_f32_e32 v134, v30, v30
	v_add_f32_e32 v135, v26, v132
	v_mov_b32_e32 v132, v26
	v_mov_b32_e32 v133, v33
	v_fmac_f32_e32 v134, v32, v32
	v_pk_mul_f32 v[132:133], v[132:133], v[132:133]
	s_nop 0
	v_add_f32_e32 v133, v133, v134
	v_add_f32_e32 v140, v132, v133
	v_add_f32_e32 v132, v27, v135
	v_add_f32_e32 v141, v28, v132
	v_pk_mul_f32 v[132:133], v[28:29], v[28:29]
	v_pk_mul_f32 v[134:135], v[26:27], v[26:27]
	s_nop 0
	v_add_f32_e32 v133, v135, v140
	v_add_f32_e32 v134, v132, v133
	v_add_f32_e32 v132, v29, v141
	v_add_f32_e32 v135, v132, v22
	v_pk_mov_b32 v[132:133], v[28:29], v[22:23] op_sel:[1,0]
	s_nop 0
	v_pk_mul_f32 v[132:133], v[132:133], v[132:133]
	s_nop 0
	v_add_f32_e32 v132, v132, v134
	v_add_f32_e32 v140, v132, v133
	v_add_f32_e32 v132, v23, v135
	v_add_f32_e32 v141, v24, v132
	v_pk_mul_f32 v[132:133], v[24:25], v[24:25]
	v_pk_mul_f32 v[134:135], v[22:23], v[22:23]
	s_nop 0
	v_add_f32_e32 v133, v135, v140
	v_add_f32_e32 v134, v132, v133
	v_add_f32_e32 v132, v25, v141
	v_add_f32_e32 v135, v18, v132
	v_mov_b32_e32 v132, v18
	v_mov_b32_e32 v133, v25
	v_pk_mul_f32 v[132:133], v[132:133], v[132:133]
	v_pk_mul_f32 v[140:141], v[18:19], v[18:19]
	v_add_f32_e32 v133, v133, v134
	v_add_f32_e32 v133, v132, v133
	v_add_f32_e32 v132, v19, v135
	v_pk_mul_f32 v[134:135], v[20:21], v[20:21]
	v_add_f32_e32 v133, v141, v133
	v_add_f32_e32 v132, v20, v132
	v_add_f32_e32 v135, v134, v133
	v_mul_f32_e32 v133, v21, v21
	v_mov_b32_e32 v134, v21
	v_pk_add_f32 v[132:133], v[134:135], v[132:133]
	v_mov_b32_e32 v134, v132
	v_mov_b32_e32 v135, v133
	s_nop 1
	v_permlane16_swap_b32_e32 v134, v132
	v_permlane16_swap_b32_e32 v135, v133
	v_pk_add_f32 v[132:133], v[132:133], v[134:135]
	v_mov_b32_e32 v134, v132
	v_mov_b32_e32 v135, v133
	s_nop 1
	v_permlane32_swap_b32_e32 v134, v132
	v_permlane32_swap_b32_e32 v135, v133
	s_and_saveexec_b64 s[26:27], s[38:39]
	s_cbranch_execz .LBB0_824
	v_pk_add_f32 v[132:133], v[132:133], v[134:135]
	ds_write_b64 v138, v[132:133] offset:5120
.LBB0_824:
	s_or_b64 exec, exec, s[26:27]
	v_add_f32_e32 v132, 0, v14
	v_add_f32_e32 v132, v15, v132
	v_add_f32_e32 v132, v16, v132
	v_mul_f32_e32 v134, v15, v15
	v_add_f32_e32 v132, v17, v132
	v_fmac_f32_e32 v134, v14, v14
	v_add_f32_e32 v135, v10, v132
	v_mov_b32_e32 v132, v10
	v_mov_b32_e32 v133, v17
	v_fmac_f32_e32 v134, v16, v16
	v_pk_mul_f32 v[132:133], v[132:133], v[132:133]
	s_nop 0
	v_add_f32_e32 v133, v133, v134
	v_add_f32_e32 v140, v132, v133
	v_add_f32_e32 v132, v11, v135
	v_add_f32_e32 v141, v12, v132
	v_pk_mul_f32 v[132:133], v[12:13], v[12:13]
	v_pk_mul_f32 v[134:135], v[10:11], v[10:11]
	s_nop 0
	v_add_f32_e32 v133, v135, v140
	v_add_f32_e32 v134, v132, v133
	v_add_f32_e32 v132, v13, v141
	v_add_f32_e32 v135, v132, v6
	v_pk_mov_b32 v[132:133], v[12:13], v[6:7] op_sel:[1,0]
	s_nop 0
	v_pk_mul_f32 v[132:133], v[132:133], v[132:133]
	s_nop 0
	v_add_f32_e32 v132, v132, v134
	v_add_f32_e32 v140, v132, v133
	v_add_f32_e32 v132, v7, v135
	v_add_f32_e32 v141, v8, v132
	v_pk_mul_f32 v[132:133], v[8:9], v[8:9]
	v_pk_mul_f32 v[134:135], v[6:7], v[6:7]
	s_nop 0
	v_add_f32_e32 v133, v135, v140
	v_add_f32_e32 v134, v132, v133
	v_add_f32_e32 v132, v9, v141
	v_add_f32_e32 v135, v2, v132
	v_mov_b32_e32 v132, v2
	v_mov_b32_e32 v133, v9
	v_pk_mul_f32 v[132:133], v[132:133], v[132:133]
	v_pk_mul_f32 v[140:141], v[2:3], v[2:3]
	v_add_f32_e32 v133, v133, v134
	v_add_f32_e32 v133, v132, v133
	v_add_f32_e32 v132, v3, v135
	v_pk_mul_f32 v[134:135], v[4:5], v[4:5]
	v_add_f32_e32 v133, v141, v133
	v_add_f32_e32 v132, v4, v132
	v_add_f32_e32 v135, v134, v133
	v_mul_f32_e32 v133, v5, v5
	v_mov_b32_e32 v134, v5
	v_pk_add_f32 v[132:133], v[134:135], v[132:133]
	v_mov_b32_e32 v134, v132
	v_mov_b32_e32 v135, v133
	s_nop 1
	v_permlane16_swap_b32_e32 v134, v132
	v_permlane16_swap_b32_e32 v135, v133
	v_pk_add_f32 v[132:133], v[132:133], v[134:135]
	v_mov_b32_e32 v134, v132
	v_mov_b32_e32 v135, v133
	s_nop 1
	v_permlane32_swap_b32_e32 v134, v132
	v_permlane32_swap_b32_e32 v135, v133
	s_and_saveexec_b64 s[26:27], s[38:39]
	s_cbranch_execz .LBB0_826
	v_pk_add_f32 v[132:133], v[132:133], v[134:135]
	ds_write_b64 v138, v[132:133] offset:5632

.LBB0_1001:
	s_mov_b64 s[66:67], s[44:45]
	v_mov_b32_e32 v190, v216
	s_ashr_i32 s65, s64, 31
	s_lshl_b64 s[68:69], s[64:65], 1
	v_ashrrev_i32_e32 v191, 31, v190
	v_lshl_add_u64 v[58:59], v[180:181], 0, s[68:69]
	v_lshlrev_b64 v[60:61], 11, v[190:191]
	v_lshl_add_u64 v[58:59], v[58:59], 0, v[60:61]
	v_add_co_u32_e32 v60, vcc, 0x10000, v58
	s_mov_b64 s[8:9], 0x8000
	s_nop 0
	v_addc_co_u32_e32 v61, vcc, 0, v59, vcc
	v_add_co_u32_e32 v74, vcc, 0x8000, v58
	v_lshl_add_u64 v[72:73], v[58:59], 0, s[8:9]
	s_nop 0
	v_addc_co_u32_e32 v75, vcc, 0, v59, vcc
	s_add_i32 s8, s96, s89
	v_add_co_u32_e32 v164, vcc, 0x18000, v58
	v_add_u32_e32 v192, s8, v190
	s_add_u32 s8, s66, s68
	v_addc_co_u32_e32 v165, vcc, 0, v59, vcc
	s_addc_u32 s9, s67, s69
	s_waitcnt vmcnt(0)
	s_barrier
	global_load_dwordx4 v[92:95], v[58:59], off
	global_load_dwordx4 v[68:71], v[58:59], off offset:256
	global_load_dwordx4 v[84:87], v[60:61], off
	global_load_dwordx4 v[62:65], v[60:61], off offset:256
	global_load_dwordx4 v[96:99], v[74:75], off
	s_nop 0
	global_load_dwordx4 v[72:75], v[72:73], off offset:256
	s_nop 0
	global_load_dwordx4 v[88:91], v[164:165], off
	global_load_dwordx4 v[58:61], v[164:165], off offset:256
	v_lshl_add_u64 v[164:165], s[8:9], 0, v[66:67]
	s_mov_b64 s[8:9], 0x8a00000
	v_ashrrev_i32_e32 v193, 31, v192
	v_lshl_add_u64 v[194:195], v[164:165], 0, s[8:9]
	v_lshlrev_b64 v[164:165], 11, v[192:193]
	v_lshl_add_u64 v[164:165], v[194:195], 0, v[164:165]
	global_load_dwordx4 v[196:199], v[164:165], off
	global_load_dwordx4 v[200:203], v[164:165], off offset:256
	v_add_u32_e32 v164, 16, v192
	v_ashrrev_i32_e32 v165, 31, v164
	v_lshlrev_b64 v[164:165], 11, v[164:165]
	v_lshl_add_u64 v[164:165], v[194:195], 0, v[164:165]
	global_load_dwordx4 v[168:171], v[164:165], off
	s_nop 0
	global_load_dwordx4 v[164:167], v[164:165], off offset:256
	v_add_u32_e32 v191, v190, v217
	s_waitcnt vmcnt(0)
	v_lshlrev_b32_e32 v208, 16, v196
	v_and_b32_e32 v209, 0xffff0000, v196
	v_lshlrev_b32_e32 v196, 16, v197
	v_and_b32_e32 v197, 0xffff0000, v197
	v_lshlrev_b32_e32 v210, 16, v198
	v_and_b32_e32 v211, 0xffff0000, v198
	v_lshlrev_b32_e32 v198, 16, v199
	v_and_b32_e32 v199, 0xffff0000, v199
	v_pk_fma_f32 v[160:161], v[208:209], s[28:29], v[160:161] op_sel_hi:[1,0,1]
	v_pk_fma_f32 v[162:163], v[196:197], s[28:29], v[162:163] op_sel_hi:[1,0,1]
	v_cvt_pk_bf16_f32 v196, v160, v161
	v_pk_fma_f32 v[156:157], v[210:211], s[28:29], v[156:157] op_sel_hi:[1,0,1]
	v_and_b32_e32 v208, 0xffff0000, v196
	v_pk_fma_f32 v[158:159], v[198:199], s[28:29], v[158:159] op_sel_hi:[1,0,1]
	v_cvt_pk_bf16_f32 v197, v162, v163
	v_cvt_pk_bf16_f32 v198, v156, v157
	v_lshlrev_b32_e32 v193, 16, v196
	v_cvt_pk_bf16_f32 v199, v158, v159
	v_lshlrev_b32_e32 v209, 16, v197
	v_and_b32_e32 v210, 0xffff0000, v197
	v_lshlrev_b32_e32 v212, 16, v198
	v_lshlrev_b32_e32 v211, 16, v199
	v_and_b32_e32 v214, 0xffff0000, v199
	v_sub_f32_e32 v220, v161, v208
	v_sub_f32_e32 v215, v162, v209
	v_sub_f32_e32 v226, v163, v210
	v_sub_f32_e32 v193, v160, v193
	v_sub_f32_e32 v227, v158, v211
	v_sub_f32_e32 v228, v159, v214
	v_mfma_f32_16x16x32_bf16 v[208:211], v[92:95], v[196:199], 0
	v_sub_f32_e32 v214, v156, v212
	v_cvt_pk_bf16_f32 v212, v193, v220
	v_and_b32_e32 v213, 0xffff0000, v198
	v_mfma_f32_16x16x32_bf16 v[220:223], v[96:99], v[196:199], 0
	v_sub_f32_e32 v229, v157, v213
	v_cvt_pk_bf16_f32 v213, v215, v226
	v_cvt_pk_bf16_f32 v214, v214, v229
	v_cvt_pk_bf16_f32 v215, v227, v228
	v_pk_add_f32 v[226:227], v[160:161], v[156:157]
	v_mfma_f32_16x16x32_bf16 v[208:211], v[92:95], v[212:215], v[208:211]
	v_add_f32_e32 v193, 0, v226
	v_pk_add_f32 v[224:225], v[162:163], v[158:159]
	v_add_f32_e32 v193, v227, v193
	v_mfma_f32_16x16x32_bf16 v[212:215], v[96:99], v[212:215], v[220:223]
	v_add_f32_e32 v193, v224, v193
	v_add_f32_e32 v193, v225, v193
	v_mfma_f32_16x16x32_bf16 v[208:211], v[84:87], v[196:199], v[208:211]
	v_mul_f32_e64 v220, v156, v156
	v_mul_f32_e64 v221, v157, v157
	v_pk_mul_f32 v[222:223], v[158:159], v[158:159]
	v_pk_fma_f32 v[220:221], v[160:161], v[160:161], v[220:221]
	v_mfma_f32_16x16x32_bf16 v[196:199], v[88:91], v[196:199], v[212:215]
	v_fma_f32 v222, v162, v162, v222
	v_fma_f32 v223, v163, v163, v223
	s_nop 0
	v_lshlrev_b32_e32 v212, 16, v200
	v_and_b32_e32 v213, 0xffff0000, v200
	v_lshlrev_b32_e32 v214, 16, v202
	v_and_b32_e32 v215, 0xffff0000, v202
	v_lshlrev_b32_e32 v200, 16, v201
	v_and_b32_e32 v201, 0xffff0000, v201
	v_pk_fma_f32 v[152:153], v[212:213], s[28:29], v[152:153] op_sel_hi:[1,0,1]
	v_pk_fma_f32 v[148:149], v[214:215], s[28:29], v[148:149] op_sel_hi:[1,0,1]
	v_pk_fma_f32 v[154:155], v[200:201], s[28:29], v[154:155] op_sel_hi:[1,0,1]
	v_pk_add_f32 v[200:201], v[152:153], v[148:149]
	v_lshlrev_b32_e32 v202, 16, v203
	v_add_f32_e32 v193, v200, v193
	v_and_b32_e32 v203, 0xffff0000, v203
	v_add_f32_e32 v224, v201, v193
	v_pk_mul_f32 v[200:201], v[152:153], v[152:153]
	v_add_f32_e32 v193, v220, v221
	v_pk_fma_f32 v[150:151], v[202:203], s[28:29], v[150:151] op_sel_hi:[1,0,1]
	v_pk_fma_f32 v[226:227], v[148:149], v[148:149], v[200:201]
	v_add_f32_e32 v193, v222, v193
	v_cvt_pk_bf16_f32 v200, v152, v153
	v_cvt_pk_bf16_f32 v201, v154, v155
	v_cvt_pk_bf16_f32 v202, v148, v149
	v_cvt_pk_bf16_f32 v203, v150, v151
	v_add_f32_e32 v193, v223, v193
	v_mfma_f32_16x16x32_bf16 v[208:211], v[68:71], v[200:203], v[208:211]
	v_and_b32_e32 v212, 0xffff0000, v200
	v_add_f32_e32 v220, v226, v193
	v_lshlrev_b32_e32 v193, 16, v200
	v_mfma_f32_16x16x32_bf16 v[196:199], v[72:75], v[200:203], v[196:199]
	v_lshlrev_b32_e32 v213, 16, v201
	v_and_b32_e32 v214, 0xffff0000, v201
	v_lshlrev_b32_e32 v215, 16, v202
	v_and_b32_e32 v221, 0xffff0000, v202
	v_lshlrev_b32_e32 v222, 16, v203
	v_and_b32_e32 v223, 0xffff0000, v203
	v_sub_f32_e32 v212, v153, v212
	v_sub_f32_e32 v213, v154, v213
	v_sub_f32_e32 v214, v155, v214
	v_sub_f32_e32 v193, v152, v193
	v_sub_f32_e32 v222, v150, v222
	v_sub_f32_e32 v223, v151, v223
	v_sub_f32_e32 v215, v148, v215
	v_sub_f32_e32 v221, v149, v221
	v_cvt_pk_bf16_f32 v212, v193, v212
	v_cvt_pk_bf16_f32 v213, v213, v214
	v_cvt_pk_bf16_f32 v214, v215, v221
	v_cvt_pk_bf16_f32 v215, v222, v223
	v_pk_add_f32 v[222:223], v[226:227], v[220:221] op_sel_hi:[1,0]
	v_mfma_f32_16x16x32_bf16 v[208:211], v[68:71], v[212:215], v[208:211]
	v_mov_b32_e32 v220, v154
	v_mov_b32_e32 v221, v150
	v_mov_b32_e32 v222, v151
	v_mfma_f32_16x16x32_bf16 v[196:199], v[72:75], v[212:215], v[196:199]
	v_mul_f32_e32 v212, v154, v154
	v_pk_fma_f32 v[212:213], v[220:221], v[220:221], v[212:213] op_sel_hi:[1,1,0]
	v_xor_b32_e32 v193, 16, v249
	v_and_b32_e32 v212, 64, v249
	v_add_u32_e32 v221, 64, v212
	v_mov_b32_e32 v212, v155
	v_pk_add_f32 v[212:213], v[212:213], v[222:223]
	v_pk_add_f32 v[214:215], v[154:155], v[150:151]
	v_pk_mul_f32 v[222:223], v[154:155], v[154:155]
	v_mul_f32_e32 v225, v151, v151
	v_cmp_lt_i32_e32 vcc, v193, v221
	v_mov_b32_e32 v215, v223
	v_pk_add_f32 v[214:215], v[214:215], v[224:225]
	v_cndmask_b32_e32 v193, v249, v193, vcc
	v_lshlrev_b32_e32 v220, 2, v193
	v_pk_add_f32 v[212:213], v[214:215], v[212:213]
	v_mov_b32_e32 v214, v212
	v_mov_b32_e32 v215, v213
	s_nop 1
	v_permlane16_swap_b32_e32 v214, v212
	v_permlane16_swap_b32_e32 v215, v213
	v_mfma_f32_16x16x32_bf16 v[208:211], v[62:65], v[200:203], v[208:211]
	v_lshlrev_b32_e32 v193, 5, v191
	v_add_u32_e32 v223, s92, v193
	v_mfma_f32_16x16x32_bf16 v[200:203], v[58:61], v[200:203], v[196:199]
	s_nop 4
	ds_write_b128 v223, v[208:211]
	s_nop 1
	ds_write_b128 v223, v[200:203] offset:16
	v_xor_b32_e32 v198, 32, v249
	v_cmp_lt_i32_e32 vcc, v198, v221
	s_waitcnt lgkmcnt(2)
	v_pk_add_f32 v[196:197], v[212:213], v[214:215]
	v_lshl_add_u32 v221, v190, 5, s93
	v_cndmask_b32_e32 v198, v249, v198, vcc
	v_lshlrev_b32_e32 v222, 2, v198
	v_mov_b32_e32 v198, v196
	v_mov_b32_e32 v199, v197
	s_nop 1
	v_permlane32_swap_b32_e32 v198, v196
	v_permlane32_swap_b32_e32 v199, v197
	s_and_saveexec_b64 s[26:27], s[38:39]
	s_cbranch_execz .LBB0_1003
	s_waitcnt lgkmcnt(0)
	v_pk_add_f32 v[196:197], v[196:197], v[198:199]
	ds_write_b64 v221, v[196:197]
.LBB0_1003:
	s_or_b64 exec, exec, s[26:27]
	v_lshlrev_b32_e32 v196, 16, v168
	v_and_b32_e32 v197, 0xffff0000, v168
	v_lshlrev_b32_e32 v168, 16, v169
	v_and_b32_e32 v169, 0xffff0000, v169
	s_waitcnt lgkmcnt(1)
	v_lshlrev_b32_e32 v198, 16, v170
	s_waitcnt lgkmcnt(0)
	v_and_b32_e32 v199, 0xffff0000, v170
	v_lshlrev_b32_e32 v170, 16, v171
	v_and_b32_e32 v171, 0xffff0000, v171
	v_pk_fma_f32 v[144:145], v[196:197], s[28:29], v[144:145] op_sel_hi:[1,0,1]
	v_pk_fma_f32 v[146:147], v[168:169], s[28:29], v[146:147] op_sel_hi:[1,0,1]
	v_cvt_pk_bf16_f32 v168, v144, v145
	v_pk_fma_f32 v[140:141], v[198:199], s[28:29], v[140:141] op_sel_hi:[1,0,1]
	v_and_b32_e32 v196, 0xffff0000, v168
	v_pk_fma_f32 v[142:143], v[170:171], s[28:29], v[142:143] op_sel_hi:[1,0,1]
	v_cvt_pk_bf16_f32 v169, v146, v147
	v_cvt_pk_bf16_f32 v170, v140, v141
	v_lshlrev_b32_e32 v193, 16, v168
	v_cvt_pk_bf16_f32 v171, v142, v143
	v_lshlrev_b32_e32 v197, 16, v169
	v_and_b32_e32 v198, 0xffff0000, v169
	v_lshlrev_b32_e32 v200, 16, v170
	v_lshlrev_b32_e32 v199, 16, v171
	v_and_b32_e32 v202, 0xffff0000, v171
	v_sub_f32_e32 v208, v145, v196
	v_sub_f32_e32 v203, v146, v197
	v_sub_f32_e32 v214, v147, v198
	v_sub_f32_e32 v193, v144, v193
	v_sub_f32_e32 v215, v142, v199
	v_sub_f32_e32 v224, v143, v202
	v_mfma_f32_16x16x32_bf16 v[196:199], v[92:95], v[168:171], 0
	v_sub_f32_e32 v202, v140, v200
	v_cvt_pk_bf16_f32 v200, v193, v208
	v_and_b32_e32 v201, 0xffff0000, v170
	v_mfma_f32_16x16x32_bf16 v[208:211], v[96:99], v[168:171], 0
	v_sub_f32_e32 v225, v141, v201
	v_cvt_pk_bf16_f32 v201, v203, v214
	v_cvt_pk_bf16_f32 v202, v202, v225
	v_cvt_pk_bf16_f32 v203, v215, v224
	v_pk_add_f32 v[214:215], v[144:145], v[140:141]
	v_mfma_f32_16x16x32_bf16 v[196:199], v[92:95], v[200:203], v[196:199]
	v_add_f32_e32 v193, 0, v214
	v_pk_add_f32 v[212:213], v[146:147], v[142:143]
	v_add_f32_e32 v193, v215, v193
	v_mfma_f32_16x16x32_bf16 v[200:203], v[96:99], v[200:203], v[208:211]
	v_add_f32_e32 v193, v212, v193
	v_add_f32_e32 v193, v213, v193
	v_lshlrev_b32_e32 v212, 16, v166
	v_mfma_f32_16x16x32_bf16 v[196:199], v[84:87], v[168:171], v[196:199]
	v_and_b32_e32 v213, 0xffff0000, v166
	v_pk_mul_f32 v[208:209], v[140:141], v[140:141]
	v_lshlrev_b32_e32 v214, 16, v167
	v_mfma_f32_16x16x32_bf16 v[200:203], v[88:91], v[168:171], v[200:203]
	v_lshlrev_b32_e32 v168, 16, v164
	v_and_b32_e32 v169, 0xffff0000, v164
	v_lshlrev_b32_e32 v170, 16, v165
	v_and_b32_e32 v171, 0xffff0000, v165
	v_and_b32_e32 v215, 0xffff0000, v167
	v_pk_fma_f32 v[164:165], v[168:169], s[28:29], v[136:137] op_sel_hi:[1,0,1]
	v_pk_fma_f32 v[166:167], v[212:213], s[28:29], v[132:133] op_sel_hi:[1,0,1]
	v_pk_mul_f32 v[210:211], v[142:143], v[142:143]
	v_pk_fma_f32 v[208:209], v[144:145], v[144:145], v[208:209]
	v_pk_add_f32 v[132:133], v[164:165], v[166:167]
	v_pk_fma_f32 v[210:211], v[146:147], v[146:147], v[210:211]
	v_pk_fma_f32 v[168:169], v[170:171], s[28:29], v[138:139] op_sel_hi:[1,0,1]
	v_pk_fma_f32 v[170:171], v[214:215], s[28:29], v[134:135] op_sel_hi:[1,0,1]
	v_add_f32_e32 v132, v132, v193
	v_add_f32_e32 v134, v208, v209
	v_add_f32_e32 v212, v133, v132
	v_pk_mul_f32 v[132:133], v[164:165], v[164:165]
	v_add_f32_e32 v134, v210, v134
	v_pk_fma_f32 v[132:133], v[166:167], v[166:167], v[132:133]
	v_add_f32_e32 v134, v211, v134
	v_add_f32_e32 v134, v132, v134
	v_pk_add_f32 v[208:209], v[132:133], v[134:135] op_sel_hi:[1,0]
	v_cvt_pk_bf16_f32 v136, v164, v165
	v_cvt_pk_bf16_f32 v137, v168, v169
	v_cvt_pk_bf16_f32 v138, v166, v167
	v_cvt_pk_bf16_f32 v139, v170, v171
	v_mov_b32_e32 v210, v168
	v_lshlrev_b32_e32 v132, 16, v136
	v_and_b32_e32 v133, 0xffff0000, v136
	v_lshlrev_b32_e32 v134, 16, v137
	v_and_b32_e32 v135, 0xffff0000, v137
	v_and_b32_e32 v208, 0xffff0000, v138
	v_sub_f32_e32 v215, v168, v134
	v_sub_f32_e32 v224, v169, v135
	v_sub_f32_e32 v225, v164, v132
	v_sub_f32_e32 v226, v165, v133
	v_mfma_f32_16x16x32_bf16 v[132:135], v[68:71], v[136:139], v[196:199]
	v_mov_b32_e32 v211, v170
	v_lshlrev_b32_e32 v193, 16, v138
	v_lshlrev_b32_e32 v213, 16, v139
	v_mfma_f32_16x16x32_bf16 v[200:203], v[72:75], v[136:139], v[200:203]
	v_sub_f32_e32 v198, v167, v208
	v_mul_f32_e32 v208, v168, v168
	v_and_b32_e32 v214, 0xffff0000, v139
	v_pk_fma_f32 v[210:211], v[210:211], v[210:211], v[208:209] op_sel_hi:[1,1,0]
	v_sub_f32_e32 v213, v170, v213
	v_sub_f32_e32 v214, v171, v214
	v_sub_f32_e32 v193, v166, v193
	v_cvt_pk_bf16_f32 v196, v225, v226
	v_cvt_pk_bf16_f32 v197, v215, v224
	v_cvt_pk_bf16_f32 v198, v193, v198
	v_cvt_pk_bf16_f32 v199, v213, v214
	v_mov_b32_e32 v210, v169
	v_mov_b32_e32 v208, v171
	v_mfma_f32_16x16x32_bf16 v[132:135], v[68:71], v[196:199], v[132:135]
	v_mul_f32_e32 v213, v171, v171
	v_mfma_f32_16x16x32_bf16 v[196:199], v[72:75], v[196:199], v[200:203]
	s_nop 2
	v_add_f32_e64 v200, v210, v208
	v_add_f32_e64 v201, v211, v209
	v_pk_add_f32 v[202:203], v[168:169], v[170:171]
	v_pk_mul_f32 v[208:209], v[168:169], v[168:169]
	s_nop 0
	v_mov_b32_e32 v203, v209
	v_pk_add_f32 v[202:203], v[202:203], v[212:213]
	s_nop 0
	v_pk_add_f32 v[208:209], v[202:203], v[200:201]
	v_mov_b32_e32 v210, v208
	v_mov_b32_e32 v211, v209
	s_nop 1
	v_permlane16_swap_b32_e32 v210, v208
	v_permlane16_swap_b32_e32 v211, v209
	v_mfma_f32_16x16x32_bf16 v[200:203], v[62:65], v[136:139], v[132:135]
	s_waitcnt lgkmcnt(0)
	s_nop 1
	v_pk_add_f32 v[132:133], v[208:209], v[210:211]
	v_mov_b32_e32 v134, v132
	v_mov_b32_e32 v135, v133
	s_nop 1
	v_permlane32_swap_b32_e32 v134, v132
	v_permlane32_swap_b32_e32 v135, v133
	v_mfma_f32_16x16x32_bf16 v[136:139], v[58:61], v[136:139], v[196:199]
	s_nop 0
	ds_write_b128 v223, v[200:203] offset:2048
	s_nop 5
	ds_write_b128 v223, v[136:139] offset:2064
	s_and_saveexec_b64 s[26:27], s[38:39]
	s_cbranch_execz .LBB0_1005
	s_waitcnt lgkmcnt(2)
	v_pk_add_f32 v[132:133], v[132:133], v[134:135]
	ds_write_b64 v221, v[132:133] offset:512
.LBB0_1005:
	s_or_b64 exec, exec, s[26:27]
	v_add_u32_e32 v132, 32, v192
	v_ashrrev_i32_e32 v133, 31, v132
	v_lshlrev_b64 v[132:133], 11, v[132:133]
	v_lshl_add_u64 v[132:133], v[194:195], 0, v[132:133]
	global_load_dwordx4 v[196:199], v[132:133], off
	global_load_dwordx4 v[200:203], v[132:133], off offset:256
	v_add_u32_e32 v132, 48, v192
	v_ashrrev_i32_e32 v133, 31, v132
	v_lshlrev_b64 v[132:133], 11, v[132:133]
	v_lshl_add_u64 v[132:133], v[194:195], 0, v[132:133]
	global_load_dwordx4 v[136:139], v[132:133], off
	s_waitcnt lgkmcnt(2)
	global_load_dwordx4 v[132:135], v[132:133], off offset:256
	s_waitcnt vmcnt(3)
	v_lshlrev_b32_e32 v208, 16, v196
	v_and_b32_e32 v209, 0xffff0000, v196
	v_lshlrev_b32_e32 v196, 16, v197
	v_and_b32_e32 v197, 0xffff0000, v197
	v_lshlrev_b32_e32 v210, 16, v198
	v_and_b32_e32 v211, 0xffff0000, v198
	v_lshlrev_b32_e32 v198, 16, v199
	v_and_b32_e32 v199, 0xffff0000, v199
	v_pk_fma_f32 v[128:129], v[208:209], s[28:29], v[128:129] op_sel_hi:[1,0,1]
	v_pk_fma_f32 v[130:131], v[196:197], s[28:29], v[130:131] op_sel_hi:[1,0,1]
	v_cvt_pk_bf16_f32 v196, v128, v129
	v_pk_fma_f32 v[124:125], v[210:211], s[28:29], v[124:125] op_sel_hi:[1,0,1]
	v_and_b32_e32 v208, 0xffff0000, v196
	v_pk_fma_f32 v[126:127], v[198:199], s[28:29], v[126:127] op_sel_hi:[1,0,1]
	v_cvt_pk_bf16_f32 v197, v130, v131
	v_cvt_pk_bf16_f32 v198, v124, v125
	v_lshlrev_b32_e32 v193, 16, v196
	v_cvt_pk_bf16_f32 v199, v126, v127
	v_lshlrev_b32_e32 v209, 16, v197
	v_and_b32_e32 v210, 0xffff0000, v197
	v_lshlrev_b32_e32 v212, 16, v198
	v_lshlrev_b32_e32 v211, 16, v199
	v_and_b32_e32 v214, 0xffff0000, v199
	v_sub_f32_e32 v224, v129, v208
	v_sub_f32_e32 v215, v130, v209
	v_sub_f32_e32 v230, v131, v210
	v_sub_f32_e32 v193, v128, v193
	v_sub_f32_e32 v231, v126, v211
	v_sub_f32_e32 v232, v127, v214
	v_mfma_f32_16x16x32_bf16 v[208:211], v[92:95], v[196:199], 0
	v_sub_f32_e32 v214, v124, v212
	v_cvt_pk_bf16_f32 v212, v193, v224
	v_and_b32_e32 v213, 0xffff0000, v198
	v_mfma_f32_16x16x32_bf16 v[224:227], v[96:99], v[196:199], 0
	v_sub_f32_e32 v233, v125, v213
	v_cvt_pk_bf16_f32 v213, v215, v230
	v_cvt_pk_bf16_f32 v214, v214, v233
	v_cvt_pk_bf16_f32 v215, v231, v232
	v_pk_add_f32 v[230:231], v[128:129], v[124:125]
	v_mfma_f32_16x16x32_bf16 v[208:211], v[92:95], v[212:215], v[208:211]
	v_add_f32_e32 v193, 0, v230
	v_pk_add_f32 v[228:229], v[130:131], v[126:127]
	v_add_f32_e32 v193, v231, v193
	v_mfma_f32_16x16x32_bf16 v[212:215], v[96:99], v[212:215], v[224:227]
	v_add_f32_e32 v193, v228, v193
	v_add_f32_e32 v193, v229, v193
	v_mfma_f32_16x16x32_bf16 v[208:211], v[84:87], v[196:199], v[208:211]
	v_mul_f32_e64 v224, v124, v124
	v_mul_f32_e64 v225, v125, v125
	v_pk_mul_f32 v[226:227], v[126:127], v[126:127]
	v_pk_fma_f32 v[224:225], v[128:129], v[128:129], v[224:225]
	v_mfma_f32_16x16x32_bf16 v[196:199], v[88:91], v[196:199], v[212:215]
	v_fma_f32 v226, v130, v130, v226
	v_fma_f32 v227, v131, v131, v227
	s_waitcnt vmcnt(2)
	v_lshlrev_b32_e32 v212, 16, v200
	v_and_b32_e32 v213, 0xffff0000, v200
	v_lshlrev_b32_e32 v214, 16, v202
	v_and_b32_e32 v215, 0xffff0000, v202
	v_lshlrev_b32_e32 v200, 16, v201
	v_and_b32_e32 v201, 0xffff0000, v201
	v_pk_fma_f32 v[120:121], v[212:213], s[28:29], v[120:121] op_sel_hi:[1,0,1]
	v_pk_fma_f32 v[116:117], v[214:215], s[28:29], v[116:117] op_sel_hi:[1,0,1]
	v_pk_fma_f32 v[122:123], v[200:201], s[28:29], v[122:123] op_sel_hi:[1,0,1]
	v_pk_add_f32 v[200:201], v[120:121], v[116:117]
	v_lshlrev_b32_e32 v202, 16, v203
	v_add_f32_e32 v193, v200, v193
	v_add_f32_e32 v228, v201, v193
	v_add_f32_e32 v193, v224, v225
	v_pk_mul_f32 v[200:201], v[120:121], v[120:121]
	v_add_f32_e32 v193, v226, v193
	v_and_b32_e32 v203, 0xffff0000, v203
	v_pk_fma_f32 v[200:201], v[116:117], v[116:117], v[200:201]
	v_add_f32_e32 v193, v227, v193
	v_pk_fma_f32 v[118:119], v[202:203], s[28:29], v[118:119] op_sel_hi:[1,0,1]
	v_add_f32_e32 v202, v200, v193
	v_pk_add_f32 v[224:225], v[200:201], v[202:203] op_sel_hi:[1,0]
	v_cvt_pk_bf16_f32 v201, v122, v123
	v_cvt_pk_bf16_f32 v202, v116, v117
	v_cvt_pk_bf16_f32 v200, v120, v121
	v_cvt_pk_bf16_f32 v203, v118, v119
	v_mov_b32_e32 v226, v122
	v_lshlrev_b32_e32 v213, 16, v201
	v_and_b32_e32 v214, 0xffff0000, v201
	v_and_b32_e32 v224, 0xffff0000, v202
	v_lshlrev_b32_e32 v215, 16, v202
	v_sub_f32_e32 v213, v122, v213
	v_sub_f32_e32 v214, v123, v214
	v_mfma_f32_16x16x32_bf16 v[208:211], v[68:71], v[200:203], v[208:211]
	v_sub_f32_e32 v224, v117, v224
	v_mov_b32_e32 v227, v118
	v_and_b32_e32 v212, 0xffff0000, v200
	v_mfma_f32_16x16x32_bf16 v[196:199], v[72:75], v[200:203], v[196:199]
	v_sub_f32_e32 v215, v116, v215
	v_cvt_pk_bf16_f32 v213, v213, v214
	v_cvt_pk_bf16_f32 v214, v215, v224
	v_mul_f32_e32 v224, v122, v122
	v_lshlrev_b32_e32 v193, 16, v200
	v_lshlrev_b32_e32 v229, 16, v203
	v_and_b32_e32 v230, 0xffff0000, v203
	v_sub_f32_e32 v212, v121, v212
	v_pk_fma_f32 v[226:227], v[226:227], v[226:227], v[224:225] op_sel_hi:[1,1,0]
	v_sub_f32_e32 v193, v120, v193
	v_sub_f32_e32 v229, v118, v229
	v_sub_f32_e32 v230, v119, v230
	v_cvt_pk_bf16_f32 v212, v193, v212
	v_cvt_pk_bf16_f32 v215, v229, v230
	v_mov_b32_e32 v226, v123
	v_mov_b32_e32 v224, v119
	v_mfma_f32_16x16x32_bf16 v[208:211], v[68:71], v[212:215], v[208:211]
	v_mul_f32_e32 v229, v119, v119
	v_mfma_f32_16x16x32_bf16 v[212:215], v[72:75], v[212:215], v[196:199]
	s_nop 2
	v_add_f32_e64 v196, v226, v224
	v_add_f32_e64 v197, v227, v225
	v_pk_add_f32 v[198:199], v[122:123], v[118:119]
	v_pk_mul_f32 v[224:225], v[122:123], v[122:123]
	v_mfma_f32_16x16x32_bf16 v[208:211], v[62:65], v[200:203], v[208:211]
	v_mov_b32_e32 v199, v225
	v_pk_add_f32 v[198:199], v[198:199], v[228:229]
	s_nop 0
	v_pk_add_f32 v[196:197], v[198:199], v[196:197]
	v_mov_b32_e32 v198, v196
	v_mov_b32_e32 v199, v197
	s_nop 1
	v_permlane16_swap_b32_e32 v198, v196
	v_permlane16_swap_b32_e32 v199, v197
	v_mfma_f32_16x16x32_bf16 v[200:203], v[58:61], v[200:203], v[212:215]
	s_nop 0
	ds_write_b128 v223, v[208:211] offset:4096
	s_nop 5
	ds_write_b128 v223, v[200:203] offset:4112
	s_waitcnt lgkmcnt(2)
	v_pk_add_f32 v[196:197], v[196:197], v[198:199]
	v_mov_b32_e32 v198, v196
	v_mov_b32_e32 v199, v197
	s_nop 1
	v_permlane32_swap_b32_e32 v198, v196
	v_permlane32_swap_b32_e32 v199, v197
	s_and_saveexec_b64 s[26:27], s[38:39]
	s_cbranch_execz .LBB0_1007
	s_waitcnt lgkmcnt(0)
	v_pk_add_f32 v[196:197], v[196:197], v[198:199]
	ds_write_b64 v221, v[196:197] offset:1024
.LBB0_1007:
	s_or_b64 exec, exec, s[26:27]
	s_waitcnt vmcnt(1)
	v_lshlrev_b32_e32 v196, 16, v136
	v_and_b32_e32 v197, 0xffff0000, v136
	v_lshlrev_b32_e32 v136, 16, v137
	v_and_b32_e32 v137, 0xffff0000, v137
	s_waitcnt lgkmcnt(1)
	v_lshlrev_b32_e32 v198, 16, v138
	s_waitcnt lgkmcnt(0)
	v_and_b32_e32 v199, 0xffff0000, v138
	v_lshlrev_b32_e32 v138, 16, v139
	v_and_b32_e32 v139, 0xffff0000, v139
	v_pk_fma_f32 v[112:113], v[196:197], s[28:29], v[112:113] op_sel_hi:[1,0,1]
	v_pk_fma_f32 v[114:115], v[136:137], s[28:29], v[114:115] op_sel_hi:[1,0,1]
	v_cvt_pk_bf16_f32 v136, v112, v113
	v_pk_fma_f32 v[108:109], v[198:199], s[28:29], v[108:109] op_sel_hi:[1,0,1]
	v_and_b32_e32 v196, 0xffff0000, v136
	v_pk_fma_f32 v[110:111], v[138:139], s[28:29], v[110:111] op_sel_hi:[1,0,1]
	v_cvt_pk_bf16_f32 v137, v114, v115
	v_cvt_pk_bf16_f32 v138, v108, v109
	v_lshlrev_b32_e32 v193, 16, v136
	v_cvt_pk_bf16_f32 v139, v110, v111
	v_lshlrev_b32_e32 v197, 16, v137
	v_and_b32_e32 v198, 0xffff0000, v137
	v_lshlrev_b32_e32 v200, 16, v138
	v_lshlrev_b32_e32 v199, 16, v139
	v_and_b32_e32 v202, 0xffff0000, v139
	v_sub_f32_e32 v208, v113, v196
	v_sub_f32_e32 v203, v114, v197
	v_sub_f32_e32 v214, v115, v198
	v_sub_f32_e32 v193, v112, v193
	v_sub_f32_e32 v215, v110, v199
	v_sub_f32_e32 v224, v111, v202
	v_mfma_f32_16x16x32_bf16 v[196:199], v[92:95], v[136:139], 0
	v_sub_f32_e32 v202, v108, v200
	v_cvt_pk_bf16_f32 v200, v193, v208
	v_and_b32_e32 v201, 0xffff0000, v138
	v_mfma_f32_16x16x32_bf16 v[208:211], v[96:99], v[136:139], 0
	v_sub_f32_e32 v225, v109, v201
	v_cvt_pk_bf16_f32 v201, v203, v214
	v_cvt_pk_bf16_f32 v202, v202, v225
	v_cvt_pk_bf16_f32 v203, v215, v224
	v_pk_add_f32 v[214:215], v[112:113], v[108:109]
	v_mfma_f32_16x16x32_bf16 v[196:199], v[92:95], v[200:203], v[196:199]
	v_add_f32_e32 v193, 0, v214
	v_pk_add_f32 v[212:213], v[114:115], v[110:111]
	v_add_f32_e32 v193, v215, v193
	v_mfma_f32_16x16x32_bf16 v[200:203], v[96:99], v[200:203], v[208:211]
	v_add_f32_e32 v193, v212, v193
	v_add_f32_e32 v193, v213, v193
	s_waitcnt vmcnt(0)
	v_lshlrev_b32_e32 v212, 16, v134
	v_mfma_f32_16x16x32_bf16 v[196:199], v[84:87], v[136:139], v[196:199]
	v_and_b32_e32 v213, 0xffff0000, v134
	v_pk_mul_f32 v[208:209], v[108:109], v[108:109]
	v_lshlrev_b32_e32 v214, 16, v135
	v_mfma_f32_16x16x32_bf16 v[200:203], v[88:91], v[136:139], v[200:203]
	v_lshlrev_b32_e32 v136, 16, v132
	v_and_b32_e32 v137, 0xffff0000, v132
	v_lshlrev_b32_e32 v138, 16, v133
	v_and_b32_e32 v139, 0xffff0000, v133
	v_and_b32_e32 v215, 0xffff0000, v135
	v_pk_fma_f32 v[132:133], v[136:137], s[28:29], v[104:105] op_sel_hi:[1,0,1]
	v_pk_fma_f32 v[134:135], v[212:213], s[28:29], v[100:101] op_sel_hi:[1,0,1]
	v_pk_mul_f32 v[210:211], v[110:111], v[110:111]
	v_pk_fma_f32 v[208:209], v[112:113], v[112:113], v[208:209]
	v_pk_add_f32 v[100:101], v[132:133], v[134:135]
	v_pk_fma_f32 v[210:211], v[114:115], v[114:115], v[210:211]
	v_pk_fma_f32 v[136:137], v[138:139], s[28:29], v[106:107] op_sel_hi:[1,0,1]
	v_pk_fma_f32 v[138:139], v[214:215], s[28:29], v[102:103] op_sel_hi:[1,0,1]
	v_add_f32_e32 v100, v100, v193
	v_add_f32_e32 v102, v208, v209
	v_add_f32_e32 v212, v101, v100
	v_pk_mul_f32 v[100:101], v[132:133], v[132:133]
	v_add_f32_e32 v102, v210, v102
	v_pk_fma_f32 v[100:101], v[134:135], v[134:135], v[100:101]
	v_add_f32_e32 v102, v211, v102
	v_add_f32_e32 v102, v100, v102
	v_pk_add_f32 v[208:209], v[100:101], v[102:103] op_sel_hi:[1,0]
	v_cvt_pk_bf16_f32 v104, v132, v133
	v_cvt_pk_bf16_f32 v105, v136, v137
	v_cvt_pk_bf16_f32 v106, v134, v135
	v_cvt_pk_bf16_f32 v107, v138, v139
	v_mov_b32_e32 v210, v136
	v_lshlrev_b32_e32 v100, 16, v104
	v_and_b32_e32 v101, 0xffff0000, v104
	v_lshlrev_b32_e32 v102, 16, v105
	v_and_b32_e32 v103, 0xffff0000, v105
	v_and_b32_e32 v208, 0xffff0000, v106
	v_sub_f32_e32 v215, v136, v102
	v_sub_f32_e32 v224, v137, v103
	v_sub_f32_e32 v225, v132, v100
	v_sub_f32_e32 v226, v133, v101
	v_mfma_f32_16x16x32_bf16 v[100:103], v[68:71], v[104:107], v[196:199]
	v_mov_b32_e32 v211, v138
	v_lshlrev_b32_e32 v193, 16, v106
	v_lshlrev_b32_e32 v213, 16, v107
	v_mfma_f32_16x16x32_bf16 v[200:203], v[72:75], v[104:107], v[200:203]
	v_sub_f32_e32 v198, v135, v208
	v_mul_f32_e32 v208, v136, v136
	v_and_b32_e32 v214, 0xffff0000, v107
	v_pk_fma_f32 v[210:211], v[210:211], v[210:211], v[208:209] op_sel_hi:[1,1,0]
	v_sub_f32_e32 v213, v138, v213
	v_sub_f32_e32 v214, v139, v214
	v_sub_f32_e32 v193, v134, v193
	v_cvt_pk_bf16_f32 v196, v225, v226
	v_cvt_pk_bf16_f32 v197, v215, v224
	v_cvt_pk_bf16_f32 v198, v193, v198
	v_cvt_pk_bf16_f32 v199, v213, v214
	v_mov_b32_e32 v210, v137
	v_mov_b32_e32 v208, v139
	v_mfma_f32_16x16x32_bf16 v[100:103], v[68:71], v[196:199], v[100:103]
	v_mul_f32_e32 v213, v139, v139
	v_mfma_f32_16x16x32_bf16 v[196:199], v[72:75], v[196:199], v[200:203]
	s_nop 2
	v_add_f32_e64 v200, v210, v208
	v_add_f32_e64 v201, v211, v209
	v_pk_add_f32 v[202:203], v[136:137], v[138:139]
	v_pk_mul_f32 v[208:209], v[136:137], v[136:137]
	s_nop 0
	v_mov_b32_e32 v203, v209
	v_pk_add_f32 v[202:203], v[202:203], v[212:213]
	s_nop 0
	v_pk_add_f32 v[208:209], v[202:203], v[200:201]
	v_mov_b32_e32 v210, v208
	v_mov_b32_e32 v211, v209
	s_nop 1
	v_permlane16_swap_b32_e32 v210, v208
	v_permlane16_swap_b32_e32 v211, v209
	v_mfma_f32_16x16x32_bf16 v[200:203], v[62:65], v[104:107], v[100:103]
	s_waitcnt lgkmcnt(0)
	s_nop 1
	v_pk_add_f32 v[100:101], v[208:209], v[210:211]
	v_mov_b32_e32 v102, v100
	v_mov_b32_e32 v103, v101
	s_nop 1
	v_permlane32_swap_b32_e32 v102, v100
	v_permlane32_swap_b32_e32 v103, v101
	v_mfma_f32_16x16x32_bf16 v[104:107], v[58:61], v[104:107], v[196:199]
	s_nop 0
	ds_write_b128 v223, v[200:203] offset:6144
	s_nop 5
	ds_write_b128 v223, v[104:107] offset:6160
	s_and_saveexec_b64 s[26:27], s[38:39]
	s_cbranch_execz .LBB0_1009
	s_waitcnt lgkmcnt(2)
	v_pk_add_f32 v[100:101], v[100:101], v[102:103]
	ds_write_b64 v221, v[100:101] offset:1536
.LBB0_1009:
	s_or_b64 exec, exec, s[26:27]
	v_add_u32_e32 v100, 0x80, v192
	v_ashrrev_i32_e32 v101, 31, v100
	v_lshlrev_b64 v[100:101], 11, v[100:101]
	v_lshl_add_u64 v[100:101], v[194:195], 0, v[100:101]
	global_load_dwordx4 v[196:199], v[100:101], off
	global_load_dwordx4 v[200:203], v[100:101], off offset:256
	v_add_u32_e32 v100, 0x90, v192
	v_ashrrev_i32_e32 v101, 31, v100
	v_lshlrev_b64 v[100:101], 11, v[100:101]
	v_lshl_add_u64 v[100:101], v[194:195], 0, v[100:101]
	global_load_dwordx4 v[104:107], v[100:101], off
	s_waitcnt lgkmcnt(2)
	global_load_dwordx4 v[100:103], v[100:101], off offset:256
	s_waitcnt vmcnt(3)
	v_lshlrev_b32_e32 v208, 16, v196
	v_and_b32_e32 v209, 0xffff0000, v196
	v_lshlrev_b32_e32 v196, 16, v197
	v_and_b32_e32 v197, 0xffff0000, v197
	v_lshlrev_b32_e32 v210, 16, v198
	v_and_b32_e32 v211, 0xffff0000, v198
	v_lshlrev_b32_e32 v198, 16, v199
	v_and_b32_e32 v199, 0xffff0000, v199
	v_pk_fma_f32 v[80:81], v[208:209], s[28:29], v[80:81] op_sel_hi:[1,0,1]
	v_pk_fma_f32 v[82:83], v[196:197], s[28:29], v[82:83] op_sel_hi:[1,0,1]
	v_cvt_pk_bf16_f32 v196, v80, v81
	v_pk_fma_f32 v[76:77], v[210:211], s[28:29], v[76:77] op_sel_hi:[1,0,1]
	v_and_b32_e32 v208, 0xffff0000, v196
	v_pk_fma_f32 v[78:79], v[198:199], s[28:29], v[78:79] op_sel_hi:[1,0,1]
	v_cvt_pk_bf16_f32 v197, v82, v83
	v_cvt_pk_bf16_f32 v198, v76, v77
	v_lshlrev_b32_e32 v193, 16, v196
	v_cvt_pk_bf16_f32 v199, v78, v79
	v_lshlrev_b32_e32 v209, 16, v197
	v_and_b32_e32 v210, 0xffff0000, v197
	v_lshlrev_b32_e32 v212, 16, v198
	v_lshlrev_b32_e32 v211, 16, v199
	v_and_b32_e32 v214, 0xffff0000, v199
	v_sub_f32_e32 v224, v81, v208
	v_sub_f32_e32 v215, v82, v209
	v_sub_f32_e32 v230, v83, v210
	v_sub_f32_e32 v193, v80, v193
	v_sub_f32_e32 v231, v78, v211
	v_sub_f32_e32 v232, v79, v214
	v_mfma_f32_16x16x32_bf16 v[208:211], v[92:95], v[196:199], 0
	v_sub_f32_e32 v214, v76, v212
	v_cvt_pk_bf16_f32 v212, v193, v224
	v_and_b32_e32 v213, 0xffff0000, v198
	v_mfma_f32_16x16x32_bf16 v[224:227], v[96:99], v[196:199], 0
	v_sub_f32_e32 v233, v77, v213
	v_cvt_pk_bf16_f32 v213, v215, v230
	v_cvt_pk_bf16_f32 v214, v214, v233
	v_cvt_pk_bf16_f32 v215, v231, v232
	v_pk_add_f32 v[230:231], v[80:81], v[76:77]
	v_mfma_f32_16x16x32_bf16 v[208:211], v[92:95], v[212:215], v[208:211]
	v_add_f32_e32 v193, 0, v230
	v_pk_add_f32 v[228:229], v[82:83], v[78:79]
	v_add_f32_e32 v193, v231, v193
	v_mfma_f32_16x16x32_bf16 v[212:215], v[96:99], v[212:215], v[224:227]
	v_add_f32_e32 v193, v228, v193
	v_add_f32_e32 v193, v229, v193
	v_mfma_f32_16x16x32_bf16 v[208:211], v[84:87], v[196:199], v[208:211]
	v_mul_f32_e64 v224, v76, v76
	v_mul_f32_e64 v225, v77, v77
	v_pk_mul_f32 v[226:227], v[78:79], v[78:79]
	v_pk_fma_f32 v[224:225], v[80:81], v[80:81], v[224:225]
	v_mfma_f32_16x16x32_bf16 v[196:199], v[88:91], v[196:199], v[212:215]
	v_fma_f32 v226, v82, v82, v226
	v_fma_f32 v227, v83, v83, v227
	s_waitcnt vmcnt(2)
	v_lshlrev_b32_e32 v212, 16, v200
	v_and_b32_e32 v213, 0xffff0000, v200
	v_lshlrev_b32_e32 v214, 16, v202
	v_and_b32_e32 v215, 0xffff0000, v202
	v_lshlrev_b32_e32 v200, 16, v201
	v_and_b32_e32 v201, 0xffff0000, v201
	v_pk_fma_f32 v[54:55], v[212:213], s[28:29], v[54:55] op_sel_hi:[1,0,1]
	v_pk_fma_f32 v[50:51], v[214:215], s[28:29], v[50:51] op_sel_hi:[1,0,1]
	v_pk_fma_f32 v[56:57], v[200:201], s[28:29], v[56:57] op_sel_hi:[1,0,1]
	v_pk_add_f32 v[200:201], v[54:55], v[50:51]
	v_lshlrev_b32_e32 v202, 16, v203
	v_add_f32_e32 v193, v200, v193
	v_add_f32_e32 v228, v201, v193
	v_add_f32_e32 v193, v224, v225
	v_pk_mul_f32 v[200:201], v[54:55], v[54:55]
	v_add_f32_e32 v193, v226, v193
	v_and_b32_e32 v203, 0xffff0000, v203
	v_pk_fma_f32 v[200:201], v[50:51], v[50:51], v[200:201]
	v_add_f32_e32 v193, v227, v193
	v_pk_fma_f32 v[52:53], v[202:203], s[28:29], v[52:53] op_sel_hi:[1,0,1]
	v_add_f32_e32 v202, v200, v193
	v_pk_add_f32 v[224:225], v[200:201], v[202:203] op_sel_hi:[1,0]
	v_cvt_pk_bf16_f32 v201, v56, v57
	v_cvt_pk_bf16_f32 v202, v50, v51
	v_cvt_pk_bf16_f32 v200, v54, v55
	v_cvt_pk_bf16_f32 v203, v52, v53
	v_mov_b32_e32 v226, v56
	v_lshlrev_b32_e32 v213, 16, v201
	v_and_b32_e32 v214, 0xffff0000, v201
	v_and_b32_e32 v224, 0xffff0000, v202
	v_lshlrev_b32_e32 v215, 16, v202
	v_sub_f32_e32 v213, v56, v213
	v_sub_f32_e32 v214, v57, v214
	v_mfma_f32_16x16x32_bf16 v[208:211], v[68:71], v[200:203], v[208:211]
	v_sub_f32_e32 v224, v51, v224
	v_mov_b32_e32 v227, v52
	v_and_b32_e32 v212, 0xffff0000, v200
	v_mfma_f32_16x16x32_bf16 v[196:199], v[72:75], v[200:203], v[196:199]
	v_sub_f32_e32 v215, v50, v215
	v_cvt_pk_bf16_f32 v213, v213, v214
	v_cvt_pk_bf16_f32 v214, v215, v224
	v_mul_f32_e32 v224, v56, v56
	v_lshlrev_b32_e32 v193, 16, v200
	v_lshlrev_b32_e32 v229, 16, v203
	v_and_b32_e32 v230, 0xffff0000, v203
	v_sub_f32_e32 v212, v55, v212
	v_pk_fma_f32 v[226:227], v[226:227], v[226:227], v[224:225] op_sel_hi:[1,1,0]
	v_sub_f32_e32 v193, v54, v193
	v_sub_f32_e32 v229, v52, v229
	v_sub_f32_e32 v230, v53, v230
	v_cvt_pk_bf16_f32 v212, v193, v212
	v_cvt_pk_bf16_f32 v215, v229, v230
	v_mov_b32_e32 v226, v57
	v_mov_b32_e32 v224, v53
	v_mfma_f32_16x16x32_bf16 v[208:211], v[68:71], v[212:215], v[208:211]
	v_mul_f32_e32 v229, v53, v53
	v_mfma_f32_16x16x32_bf16 v[212:215], v[72:75], v[212:215], v[196:199]
	s_nop 2
	v_add_f32_e64 v196, v226, v224
	v_add_f32_e64 v197, v227, v225
	v_pk_add_f32 v[198:199], v[56:57], v[52:53]
	v_pk_mul_f32 v[224:225], v[56:57], v[56:57]
	v_mfma_f32_16x16x32_bf16 v[208:211], v[62:65], v[200:203], v[208:211]
	v_mov_b32_e32 v199, v225
	v_pk_add_f32 v[198:199], v[198:199], v[228:229]
	s_nop 0
	v_pk_add_f32 v[196:197], v[198:199], v[196:197]
	v_mov_b32_e32 v198, v196
	v_mov_b32_e32 v199, v197
	s_nop 1
	v_permlane16_swap_b32_e32 v198, v196
	v_permlane16_swap_b32_e32 v199, v197
	v_mfma_f32_16x16x32_bf16 v[200:203], v[58:61], v[200:203], v[212:215]
	s_nop 0
	ds_write_b128 v223, v[208:211] offset:16384
	s_nop 5
	ds_write_b128 v223, v[200:203] offset:16400
	s_waitcnt lgkmcnt(2)
	v_pk_add_f32 v[196:197], v[196:197], v[198:199]
	v_mov_b32_e32 v198, v196
	v_mov_b32_e32 v199, v197
	s_nop 1
	v_permlane32_swap_b32_e32 v198, v196
	v_permlane32_swap_b32_e32 v199, v197
	s_and_saveexec_b64 s[26:27], s[38:39]
	s_cbranch_execz .LBB0_1011
	s_waitcnt lgkmcnt(0)
	v_pk_add_f32 v[196:197], v[196:197], v[198:199]
	ds_write_b64 v221, v[196:197] offset:4096
.LBB0_1011:
	s_or_b64 exec, exec, s[26:27]
	s_waitcnt vmcnt(1)
	v_lshlrev_b32_e32 v196, 16, v104
	v_and_b32_e32 v197, 0xffff0000, v104
	v_lshlrev_b32_e32 v104, 16, v105
	v_and_b32_e32 v105, 0xffff0000, v105
	s_waitcnt lgkmcnt(1)
	v_lshlrev_b32_e32 v198, 16, v106
	s_waitcnt lgkmcnt(0)
	v_and_b32_e32 v199, 0xffff0000, v106
	v_lshlrev_b32_e32 v106, 16, v107
	v_and_b32_e32 v107, 0xffff0000, v107
	v_pk_fma_f32 v[46:47], v[196:197], s[28:29], v[46:47] op_sel_hi:[1,0,1]
	v_pk_fma_f32 v[48:49], v[104:105], s[28:29], v[48:49] op_sel_hi:[1,0,1]
	v_cvt_pk_bf16_f32 v104, v46, v47
	v_pk_fma_f32 v[42:43], v[198:199], s[28:29], v[42:43] op_sel_hi:[1,0,1]
	v_and_b32_e32 v196, 0xffff0000, v104
	v_pk_fma_f32 v[44:45], v[106:107], s[28:29], v[44:45] op_sel_hi:[1,0,1]
	v_cvt_pk_bf16_f32 v105, v48, v49
	v_cvt_pk_bf16_f32 v106, v42, v43
	v_lshlrev_b32_e32 v193, 16, v104
	v_cvt_pk_bf16_f32 v107, v44, v45
	v_lshlrev_b32_e32 v197, 16, v105
	v_and_b32_e32 v198, 0xffff0000, v105
	v_lshlrev_b32_e32 v200, 16, v106
	v_lshlrev_b32_e32 v199, 16, v107
	v_and_b32_e32 v202, 0xffff0000, v107
	v_sub_f32_e32 v208, v47, v196
	v_sub_f32_e32 v203, v48, v197
	v_sub_f32_e32 v214, v49, v198
	v_sub_f32_e32 v193, v46, v193
	v_sub_f32_e32 v215, v44, v199
	v_sub_f32_e32 v224, v45, v202
	v_mfma_f32_16x16x32_bf16 v[196:199], v[92:95], v[104:107], 0
	v_sub_f32_e32 v202, v42, v200
	v_cvt_pk_bf16_f32 v200, v193, v208
	v_and_b32_e32 v201, 0xffff0000, v106
	v_mfma_f32_16x16x32_bf16 v[208:211], v[96:99], v[104:107], 0
	v_sub_f32_e32 v225, v43, v201
	v_cvt_pk_bf16_f32 v201, v203, v214
	v_cvt_pk_bf16_f32 v202, v202, v225
	v_cvt_pk_bf16_f32 v203, v215, v224
	v_pk_add_f32 v[214:215], v[46:47], v[42:43]
	v_mfma_f32_16x16x32_bf16 v[196:199], v[92:95], v[200:203], v[196:199]
	v_add_f32_e32 v193, 0, v214
	v_pk_add_f32 v[212:213], v[48:49], v[44:45]
	v_add_f32_e32 v193, v215, v193
	v_mfma_f32_16x16x32_bf16 v[200:203], v[96:99], v[200:203], v[208:211]
	v_add_f32_e32 v193, v212, v193
	v_add_f32_e32 v193, v213, v193
	s_waitcnt vmcnt(0)
	v_lshlrev_b32_e32 v212, 16, v102
	v_mfma_f32_16x16x32_bf16 v[196:199], v[84:87], v[104:107], v[196:199]
	v_and_b32_e32 v213, 0xffff0000, v102
	v_pk_mul_f32 v[208:209], v[42:43], v[42:43]
	v_lshlrev_b32_e32 v214, 16, v103
	v_mfma_f32_16x16x32_bf16 v[200:203], v[88:91], v[104:107], v[200:203]
	v_lshlrev_b32_e32 v104, 16, v100
	v_and_b32_e32 v105, 0xffff0000, v100
	v_lshlrev_b32_e32 v106, 16, v101
	v_and_b32_e32 v107, 0xffff0000, v101
	v_and_b32_e32 v215, 0xffff0000, v103
	v_pk_fma_f32 v[100:101], v[104:105], s[28:29], v[38:39] op_sel_hi:[1,0,1]
	v_pk_fma_f32 v[102:103], v[212:213], s[28:29], v[34:35] op_sel_hi:[1,0,1]
	v_pk_mul_f32 v[210:211], v[44:45], v[44:45]
	v_pk_fma_f32 v[208:209], v[46:47], v[46:47], v[208:209]
	v_pk_add_f32 v[34:35], v[100:101], v[102:103]
	v_pk_fma_f32 v[210:211], v[48:49], v[48:49], v[210:211]
	v_pk_fma_f32 v[104:105], v[106:107], s[28:29], v[40:41] op_sel_hi:[1,0,1]
	v_pk_fma_f32 v[106:107], v[214:215], s[28:29], v[36:37] op_sel_hi:[1,0,1]
	v_add_f32_e32 v34, v34, v193
	v_add_f32_e32 v36, v208, v209
	v_add_f32_e32 v212, v35, v34
	v_pk_mul_f32 v[34:35], v[100:101], v[100:101]
	v_add_f32_e32 v36, v210, v36
	v_pk_fma_f32 v[34:35], v[102:103], v[102:103], v[34:35]
	v_add_f32_e32 v36, v211, v36
	v_add_f32_e32 v36, v34, v36
	v_pk_add_f32 v[208:209], v[34:35], v[36:37] op_sel_hi:[1,0]
	v_cvt_pk_bf16_f32 v38, v100, v101
	v_cvt_pk_bf16_f32 v39, v104, v105
	v_cvt_pk_bf16_f32 v40, v102, v103
	v_cvt_pk_bf16_f32 v41, v106, v107
	v_mov_b32_e32 v210, v104
	v_lshlrev_b32_e32 v34, 16, v38
	v_and_b32_e32 v35, 0xffff0000, v38
	v_lshlrev_b32_e32 v36, 16, v39
	v_and_b32_e32 v37, 0xffff0000, v39
	v_and_b32_e32 v208, 0xffff0000, v40
	v_sub_f32_e32 v215, v104, v36
	v_sub_f32_e32 v224, v105, v37
	v_sub_f32_e32 v225, v100, v34
	v_sub_f32_e32 v226, v101, v35
	v_mfma_f32_16x16x32_bf16 v[34:37], v[68:71], v[38:41], v[196:199]
	v_mov_b32_e32 v211, v106
	v_lshlrev_b32_e32 v193, 16, v40
	v_lshlrev_b32_e32 v213, 16, v41
	v_mfma_f32_16x16x32_bf16 v[200:203], v[72:75], v[38:41], v[200:203]
	v_sub_f32_e32 v198, v103, v208
	v_mul_f32_e32 v208, v104, v104
	v_and_b32_e32 v214, 0xffff0000, v41
	v_pk_fma_f32 v[210:211], v[210:211], v[210:211], v[208:209] op_sel_hi:[1,1,0]
	v_sub_f32_e32 v213, v106, v213
	v_sub_f32_e32 v214, v107, v214
	v_sub_f32_e32 v193, v102, v193
	v_cvt_pk_bf16_f32 v196, v225, v226
	v_cvt_pk_bf16_f32 v197, v215, v224
	v_cvt_pk_bf16_f32 v198, v193, v198
	v_cvt_pk_bf16_f32 v199, v213, v214
	v_mov_b32_e32 v210, v105
	v_mov_b32_e32 v208, v107
	v_mfma_f32_16x16x32_bf16 v[34:37], v[68:71], v[196:199], v[34:37]
	v_mul_f32_e32 v213, v107, v107
	v_mfma_f32_16x16x32_bf16 v[196:199], v[72:75], v[196:199], v[200:203]
	s_nop 2
	v_add_f32_e64 v200, v210, v208
	v_add_f32_e64 v201, v211, v209
	v_pk_add_f32 v[202:203], v[104:105], v[106:107]
	v_pk_mul_f32 v[208:209], v[104:105], v[104:105]
	s_nop 0
	v_mov_b32_e32 v203, v209
	v_pk_add_f32 v[202:203], v[202:203], v[212:213]
	s_nop 0
	v_pk_add_f32 v[208:209], v[202:203], v[200:201]
	v_mov_b32_e32 v210, v208
	v_mov_b32_e32 v211, v209
	s_nop 1
	v_permlane16_swap_b32_e32 v210, v208
	v_permlane16_swap_b32_e32 v211, v209
	v_mfma_f32_16x16x32_bf16 v[200:203], v[62:65], v[38:41], v[34:37]
	s_waitcnt lgkmcnt(0)
	s_nop 1
	v_pk_add_f32 v[34:35], v[208:209], v[210:211]
	v_mov_b32_e32 v36, v34
	v_mov_b32_e32 v37, v35
	s_nop 1
	v_permlane32_swap_b32_e32 v36, v34
	v_permlane32_swap_b32_e32 v37, v35
	v_mfma_f32_16x16x32_bf16 v[38:41], v[58:61], v[38:41], v[196:199]
	s_nop 0
	ds_write_b128 v223, v[200:203] offset:18432
	s_nop 5
	ds_write_b128 v223, v[38:41] offset:18448
	s_and_saveexec_b64 s[26:27], s[38:39]
	s_cbranch_execz .LBB0_1013
	s_waitcnt lgkmcnt(2)
	v_pk_add_f32 v[34:35], v[34:35], v[36:37]
	ds_write_b64 v221, v[34:35] offset:4608
.LBB0_1013:
	s_or_b64 exec, exec, s[26:27]
	v_add_u32_e32 v34, 0xa0, v192
	v_ashrrev_i32_e32 v35, 31, v34
	v_lshlrev_b64 v[34:35], 11, v[34:35]
	v_lshl_add_u64 v[34:35], v[194:195], 0, v[34:35]
	global_load_dwordx4 v[196:199], v[34:35], off
	global_load_dwordx4 v[200:203], v[34:35], off offset:256
	v_add_u32_e32 v34, 0xb0, v192
	v_ashrrev_i32_e32 v35, 31, v34
	v_lshlrev_b64 v[34:35], 11, v[34:35]
	v_lshl_add_u64 v[34:35], v[194:195], 0, v[34:35]
	global_load_dwordx4 v[38:41], v[34:35], off
	s_waitcnt lgkmcnt(2)
	global_load_dwordx4 v[34:37], v[34:35], off offset:256
	s_waitcnt vmcnt(3)
	v_lshlrev_b32_e32 v192, 16, v196
	v_and_b32_e32 v193, 0xffff0000, v196
	v_lshlrev_b32_e32 v194, 16, v197
	v_and_b32_e32 v195, 0xffff0000, v197
	v_lshlrev_b32_e32 v208, 16, v198
	v_and_b32_e32 v209, 0xffff0000, v198
	v_lshlrev_b32_e32 v198, 16, v199
	v_and_b32_e32 v199, 0xffff0000, v199
	v_pk_fma_f32 v[192:193], v[192:193], s[28:29], v[30:31] op_sel_hi:[1,0,1]
	v_pk_fma_f32 v[196:197], v[194:195], s[28:29], v[32:33] op_sel_hi:[1,0,1]
	v_pk_fma_f32 v[194:195], v[208:209], s[28:29], v[26:27] op_sel_hi:[1,0,1]
	v_cvt_pk_bf16_f32 v26, v192, v193
	v_pk_fma_f32 v[198:199], v[198:199], s[28:29], v[28:29] op_sel_hi:[1,0,1]
	v_lshlrev_b32_e32 v30, 16, v26
	v_and_b32_e32 v31, 0xffff0000, v26
	v_cvt_pk_bf16_f32 v27, v196, v197
	v_cvt_pk_bf16_f32 v28, v194, v195
	v_cvt_pk_bf16_f32 v29, v198, v199
	v_sub_f32_e32 v212, v192, v30
	v_lshlrev_b32_e32 v32, 16, v27
	v_and_b32_e32 v33, 0xffff0000, v27
	v_lshlrev_b32_e32 v208, 16, v28
	v_lshlrev_b32_e32 v210, 16, v29
	v_sub_f32_e32 v213, v193, v31
	v_sub_f32_e32 v226, v196, v32
	v_sub_f32_e32 v227, v197, v33
	v_sub_f32_e32 v228, v198, v210
	v_mfma_f32_16x16x32_bf16 v[30:33], v[92:95], v[26:29], 0
	v_sub_f32_e32 v210, v194, v208
	v_cvt_pk_bf16_f32 v208, v212, v213
	v_and_b32_e32 v211, 0xffff0000, v29
	v_mfma_f32_16x16x32_bf16 v[212:215], v[96:99], v[26:29], 0
	v_and_b32_e32 v209, 0xffff0000, v28
	v_sub_f32_e32 v211, v199, v211
	v_sub_f32_e32 v229, v195, v209
	v_cvt_pk_bf16_f32 v209, v226, v227
	v_cvt_pk_bf16_f32 v210, v210, v229
	v_cvt_pk_bf16_f32 v211, v228, v211
	v_pk_add_f32 v[226:227], v[192:193], v[194:195]
	v_mfma_f32_16x16x32_bf16 v[30:33], v[92:95], v[208:211], v[30:33]
	v_add_f32_e32 v226, 0, v226
	v_pk_add_f32 v[224:225], v[196:197], v[198:199]
	v_add_f32_e32 v226, v227, v226
	v_mfma_f32_16x16x32_bf16 v[208:211], v[96:99], v[208:211], v[212:215]
	v_add_f32_e32 v224, v224, v226
	v_add_f32_e32 v228, v225, v224
	s_waitcnt vmcnt(2)
	v_lshlrev_b32_e32 v224, 16, v202
	v_mfma_f32_16x16x32_bf16 v[30:33], v[84:87], v[26:29], v[30:33]
	v_and_b32_e32 v225, 0xffff0000, v202
	v_pk_mul_f32 v[212:213], v[194:195], v[194:195]
	v_lshlrev_b32_e32 v226, 16, v203
	v_mfma_f32_16x16x32_bf16 v[26:29], v[88:91], v[26:29], v[208:211]
	v_and_b32_e32 v227, 0xffff0000, v203
	v_pk_fma_f32 v[202:203], v[224:225], s[28:29], v[18:19] op_sel_hi:[1,0,1]
	v_pk_mul_f32 v[214:215], v[198:199], v[198:199]
	v_lshlrev_b32_e32 v208, 16, v200
	v_and_b32_e32 v209, 0xffff0000, v200
	v_lshlrev_b32_e32 v210, 16, v201
	v_and_b32_e32 v211, 0xffff0000, v201
	v_pk_fma_f32 v[200:201], v[208:209], s[28:29], v[22:23] op_sel_hi:[1,0,1]
	v_pk_fma_f32 v[212:213], v[192:193], v[192:193], v[212:213]
	v_pk_add_f32 v[18:19], v[200:201], v[202:203]
	v_pk_fma_f32 v[214:215], v[196:197], v[196:197], v[214:215]
	v_pk_fma_f32 v[208:209], v[210:211], s[28:29], v[24:25] op_sel_hi:[1,0,1]
	v_pk_fma_f32 v[210:211], v[226:227], s[28:29], v[20:21] op_sel_hi:[1,0,1]
	v_add_f32_e32 v18, v18, v228
	v_add_f32_e32 v20, v212, v213
	v_add_f32_e32 v224, v19, v18
	v_pk_mul_f32 v[18:19], v[200:201], v[200:201]
	v_add_f32_e32 v20, v214, v20
	v_pk_fma_f32 v[18:19], v[202:203], v[202:203], v[18:19]
	v_add_f32_e32 v20, v215, v20
	v_add_f32_e32 v20, v18, v20
	v_pk_add_f32 v[212:213], v[18:19], v[20:21] op_sel_hi:[1,0]
	v_cvt_pk_bf16_f32 v22, v200, v201
	v_cvt_pk_bf16_f32 v23, v208, v209
	v_cvt_pk_bf16_f32 v24, v202, v203
	v_cvt_pk_bf16_f32 v25, v210, v211
	v_mov_b32_e32 v214, v208
	v_lshlrev_b32_e32 v18, 16, v22
	v_and_b32_e32 v19, 0xffff0000, v22
	v_lshlrev_b32_e32 v20, 16, v23
	v_and_b32_e32 v21, 0xffff0000, v23
	v_lshlrev_b32_e32 v212, 16, v24
	v_sub_f32_e32 v228, v208, v20
	v_sub_f32_e32 v229, v209, v21
	v_sub_f32_e32 v230, v200, v18
	v_sub_f32_e32 v231, v201, v19
	v_mfma_f32_16x16x32_bf16 v[18:21], v[68:71], v[22:25], v[30:33]
	v_mov_b32_e32 v215, v210
	v_and_b32_e32 v225, 0xffff0000, v24
	v_lshlrev_b32_e32 v226, 16, v25
	v_mfma_f32_16x16x32_bf16 v[26:29], v[72:75], v[22:25], v[26:29]
	v_sub_f32_e32 v32, v202, v212
	v_mul_f32_e32 v212, v208, v208
	v_and_b32_e32 v227, 0xffff0000, v25
	v_sub_f32_e32 v33, v203, v225
	v_pk_fma_f32 v[214:215], v[214:215], v[214:215], v[212:213] op_sel_hi:[1,1,0]
	v_sub_f32_e32 v226, v210, v226
	v_sub_f32_e32 v227, v211, v227
	v_cvt_pk_bf16_f32 v30, v230, v231
	v_cvt_pk_bf16_f32 v31, v228, v229
	v_cvt_pk_bf16_f32 v32, v32, v33
	v_cvt_pk_bf16_f32 v33, v226, v227
	v_mov_b32_e32 v214, v209
	v_mov_b32_e32 v212, v211
	v_mfma_f32_16x16x32_bf16 v[18:21], v[68:71], v[30:33], v[18:21]
	v_mul_f32_e32 v225, v211, v211
	v_mfma_f32_16x16x32_bf16 v[26:29], v[72:75], v[30:33], v[26:29]
	v_add_f32_e64 v30, v214, v212
	v_add_f32_e64 v31, v215, v213
	v_pk_add_f32 v[32:33], v[208:209], v[210:211]
	v_pk_mul_f32 v[212:213], v[208:209], v[208:209]
	s_nop 0
	v_mov_b32_e32 v33, v213
	v_pk_add_f32 v[32:33], v[32:33], v[224:225]
	s_nop 0
	v_pk_add_f32 v[212:213], v[32:33], v[30:31]
	v_mov_b32_e32 v214, v212
	v_mov_b32_e32 v215, v213
	s_nop 1
	v_permlane16_swap_b32_e32 v214, v212
	v_permlane16_swap_b32_e32 v215, v213
	v_mfma_f32_16x16x32_bf16 v[30:33], v[62:65], v[22:25], v[18:21]
	s_waitcnt lgkmcnt(0)
	s_nop 1
	v_pk_add_f32 v[18:19], v[212:213], v[214:215]
	v_mov_b32_e32 v20, v18
	v_mov_b32_e32 v21, v19
	s_nop 1
	v_permlane32_swap_b32_e32 v20, v18
	v_permlane32_swap_b32_e32 v21, v19
	v_mfma_f32_16x16x32_bf16 v[22:25], v[58:61], v[22:25], v[26:29]
	s_nop 0
	ds_write_b128 v223, v[30:33] offset:20480
	s_nop 5
	ds_write_b128 v223, v[22:25] offset:20496
	s_and_saveexec_b64 s[26:27], s[38:39]
	s_cbranch_execz .LBB0_1015
	s_waitcnt lgkmcnt(2)
	v_pk_add_f32 v[18:19], v[18:19], v[20:21]
	ds_write_b64 v221, v[18:19] offset:5120
.LBB0_1015:
	s_or_b64 exec, exec, s[26:27]
	s_waitcnt vmcnt(1)
	v_lshlrev_b32_e32 v18, 16, v38
	v_and_b32_e32 v19, 0xffff0000, v38
	v_lshlrev_b32_e32 v22, 16, v40
	v_and_b32_e32 v23, 0xffff0000, v40
	s_waitcnt lgkmcnt(3)
	v_lshlrev_b32_e32 v20, 16, v39
	s_waitcnt lgkmcnt(2)
	v_and_b32_e32 v21, 0xffff0000, v39
	v_lshlrev_b32_e32 v24, 16, v41
	v_and_b32_e32 v25, 0xffff0000, v41
	v_pk_fma_f32 v[38:39], v[18:19], s[28:29], v[14:15] op_sel_hi:[1,0,1]
	v_pk_fma_f32 v[40:41], v[22:23], s[28:29], v[10:11] op_sel_hi:[1,0,1]
	v_cvt_pk_bf16_f32 v10, v38, v39
	v_pk_fma_f32 v[212:213], v[20:21], s[28:29], v[16:17] op_sel_hi:[1,0,1]
	v_lshlrev_b32_e32 v14, 16, v10
	v_and_b32_e32 v15, 0xffff0000, v10
	v_pk_fma_f32 v[214:215], v[24:25], s[28:29], v[12:13] op_sel_hi:[1,0,1]
	v_cvt_pk_bf16_f32 v11, v212, v213
	v_cvt_pk_bf16_f32 v12, v40, v41
	v_sub_f32_e32 v22, v38, v14
	v_cvt_pk_bf16_f32 v13, v214, v215
	v_lshlrev_b32_e32 v16, 16, v11
	v_and_b32_e32 v17, 0xffff0000, v11
	v_lshlrev_b32_e32 v18, 16, v12
	v_lshlrev_b32_e32 v20, 16, v13
	v_sub_f32_e32 v23, v39, v15
	v_sub_f32_e32 v28, v212, v16
	v_sub_f32_e32 v29, v213, v17
	v_sub_f32_e32 v30, v214, v20
	v_mfma_f32_16x16x32_bf16 v[14:17], v[92:95], v[10:13], 0
	v_sub_f32_e32 v20, v40, v18
	v_cvt_pk_bf16_f32 v18, v22, v23
	v_and_b32_e32 v21, 0xffff0000, v13
	v_mfma_f32_16x16x32_bf16 v[22:25], v[96:99], v[10:13], 0
	v_and_b32_e32 v19, 0xffff0000, v12
	v_sub_f32_e32 v21, v215, v21
	v_sub_f32_e32 v31, v41, v19
	v_cvt_pk_bf16_f32 v19, v28, v29
	v_cvt_pk_bf16_f32 v20, v20, v31
	v_cvt_pk_bf16_f32 v21, v30, v21
	v_pk_add_f32 v[28:29], v[38:39], v[40:41]
	v_mfma_f32_16x16x32_bf16 v[14:17], v[92:95], v[18:21], v[14:17]
	v_add_f32_e32 v28, 0, v28
	v_pk_add_f32 v[26:27], v[212:213], v[214:215]
	v_add_f32_e32 v28, v29, v28
	v_mfma_f32_16x16x32_bf16 v[18:21], v[96:99], v[18:21], v[22:25]
	v_add_f32_e32 v26, v26, v28
	v_add_f32_e32 v30, v27, v26
	s_waitcnt vmcnt(0)
	v_lshlrev_b32_e32 v26, 16, v36
	v_mfma_f32_16x16x32_bf16 v[14:17], v[84:87], v[10:13], v[14:17]
	v_and_b32_e32 v27, 0xffff0000, v36
	v_pk_mul_f32 v[22:23], v[40:41], v[40:41]
	v_lshlrev_b32_e32 v28, 16, v37
	v_mfma_f32_16x16x32_bf16 v[10:13], v[88:91], v[10:13], v[18:21]
	v_and_b32_e32 v29, 0xffff0000, v37
	v_pk_fma_f32 v[36:37], v[26:27], s[28:29], v[2:3] op_sel_hi:[1,0,1]
	v_pk_mul_f32 v[24:25], v[214:215], v[214:215]
	v_lshlrev_b32_e32 v18, 16, v34
	v_and_b32_e32 v19, 0xffff0000, v34
	v_lshlrev_b32_e32 v20, 16, v35
	v_and_b32_e32 v21, 0xffff0000, v35
	v_pk_fma_f32 v[34:35], v[18:19], s[28:29], v[6:7] op_sel_hi:[1,0,1]
	v_pk_fma_f32 v[22:23], v[38:39], v[38:39], v[22:23]
	v_pk_add_f32 v[2:3], v[34:35], v[36:37]
	v_pk_fma_f32 v[24:25], v[212:213], v[212:213], v[24:25]
	v_pk_fma_f32 v[86:87], v[28:29], s[28:29], v[4:5] op_sel_hi:[1,0,1]
	v_add_f32_e32 v2, v2, v30
	v_add_f32_e32 v4, v22, v23
	v_add_f32_e32 v18, v3, v2
	v_pk_mul_f32 v[2:3], v[34:35], v[34:35]
	v_add_f32_e32 v4, v24, v4
	v_pk_fma_f32 v[2:3], v[36:37], v[36:37], v[2:3]
	v_add_f32_e32 v4, v25, v4
	v_add_f32_e32 v4, v2, v4
	v_pk_fma_f32 v[84:85], v[20:21], s[28:29], v[8:9] op_sel_hi:[1,0,1]
	v_pk_add_f32 v[20:21], v[2:3], v[4:5] op_sel_hi:[1,0]
	v_cvt_pk_bf16_f32 v6, v34, v35
	v_cvt_pk_bf16_f32 v7, v84, v85
	v_cvt_pk_bf16_f32 v8, v36, v37
	v_cvt_pk_bf16_f32 v9, v86, v87
	v_mov_b32_e32 v22, v84
	v_lshlrev_b32_e32 v2, 16, v6
	v_and_b32_e32 v3, 0xffff0000, v6
	v_lshlrev_b32_e32 v4, 16, v7
	v_and_b32_e32 v5, 0xffff0000, v7
	v_and_b32_e32 v20, 0xffff0000, v8
	v_sub_f32_e32 v26, v84, v4
	v_sub_f32_e32 v27, v85, v5
	v_sub_f32_e32 v28, v34, v2
	v_sub_f32_e32 v29, v35, v3
	v_mfma_f32_16x16x32_bf16 v[2:5], v[68:71], v[6:9], v[14:17]
	v_mov_b32_e32 v23, v86
	v_lshlrev_b32_e32 v19, 16, v8
	v_lshlrev_b32_e32 v24, 16, v9
	v_mfma_f32_16x16x32_bf16 v[10:13], v[72:75], v[6:9], v[10:13]
	v_sub_f32_e32 v17, v37, v20
	v_mul_f32_e32 v20, v84, v84
	v_and_b32_e32 v25, 0xffff0000, v9
	v_sub_f32_e32 v16, v36, v19
	v_pk_fma_f32 v[22:23], v[22:23], v[22:23], v[20:21] op_sel_hi:[1,1,0]
	v_sub_f32_e32 v24, v86, v24
	v_sub_f32_e32 v25, v87, v25
	v_cvt_pk_bf16_f32 v14, v28, v29
	v_cvt_pk_bf16_f32 v15, v26, v27
	v_cvt_pk_bf16_f32 v16, v16, v17
	v_cvt_pk_bf16_f32 v17, v24, v25
	v_mov_b32_e32 v22, v85
	v_mov_b32_e32 v20, v87
	v_mfma_f32_16x16x32_bf16 v[2:5], v[68:71], v[14:17], v[2:5]
	v_mul_f32_e32 v19, v87, v87
	v_mfma_f32_16x16x32_bf16 v[10:13], v[72:75], v[14:17], v[10:13]
	v_add_f32_e64 v14, v22, v20
	v_add_f32_e64 v15, v23, v21
	v_pk_add_f32 v[16:17], v[84:85], v[86:87]
	v_pk_mul_f32 v[20:21], v[84:85], v[84:85]
	s_nop 0
	v_mov_b32_e32 v17, v21
	v_pk_add_f32 v[16:17], v[16:17], v[18:19]
	s_nop 0
	v_pk_add_f32 v[18:19], v[16:17], v[14:15]
	v_mov_b32_e32 v20, v18
	v_mov_b32_e32 v21, v19
	s_nop 1
	v_permlane16_swap_b32_e32 v20, v18
	v_permlane16_swap_b32_e32 v21, v19
	v_mfma_f32_16x16x32_bf16 v[14:17], v[62:65], v[6:9], v[2:5]
	s_waitcnt lgkmcnt(0)
	s_nop 1
	v_pk_add_f32 v[2:3], v[18:19], v[20:21]
	v_mov_b32_e32 v4, v2
	v_mov_b32_e32 v5, v3
	s_nop 1
	v_permlane32_swap_b32_e32 v4, v2
	v_permlane32_swap_b32_e32 v5, v3
	v_mfma_f32_16x16x32_bf16 v[6:9], v[58:61], v[6:9], v[10:13]
	s_nop 0
	ds_write_b128 v223, v[14:17] offset:22528
	s_nop 5
	ds_write_b128 v223, v[6:9] offset:22544
	s_and_saveexec_b64 s[26:27], s[38:39]
	s_cbranch_execz .LBB0_1017
	s_waitcnt lgkmcnt(2)
	v_pk_add_f32 v[2:3], v[2:3], v[4:5]
	ds_write_b64 v221, v[2:3] offset:5632
